# v57 plus nt hint on the stores of the converted (bf16 / e4m3) weights
# baseline (speedup 1.0000x reference)
.LBB0_20:
	s_cmpk_gt_i32 s11, 0x64f
	s_mov_b64 s[2:3], -1
	s_cbranch_scc0 .LBB0_42
	s_cmpk_gt_u32 s11, 0xe4f
	s_cbranch_scc0 .LBB0_39
	s_cmpk_gt_u32 s11, 0x124f
	s_cbranch_scc0 .LBB0_36
	s_cmpk_gt_u32 s11, 0x144f
	s_cbranch_scc0 .LBB0_33
	s_cmpk_gt_u32 s11, 0x14af
	s_cbranch_scc0 .LBB0_30
	s_cmpk_gt_u32 s11, 0x14ef
	s_cbranch_scc0 .LBB0_27
	v_readlane_b32 s2, v254, 15
	v_lshlrev_b32_e32 v160, 2, v0
	v_add_u32_e32 v86, 0x18c0, v37
	v_mov_b32_e32 v47, s2
	v_readlane_b32 s2, v254, 16
	ds_read_b32 v47, v47
	v_add_u32_e32 v87, 0x18c8, v37
	v_mov_b32_e32 v48, s2
	ds_read_b32 v48, v48
	s_lshl_b64 s[2:3], s[18:19], 2
	s_waitcnt lgkmcnt(1)
	v_readfirstlane_b32 s22, v47
	v_add_u32_e32 v47, 0x14a8, v37
	v_add_u32_e32 v88, 0x1ce0, v37
	s_waitcnt lgkmcnt(0)
	v_readfirstlane_b32 s23, v48
	s_add_u32 s22, s22, s2
	s_addc_u32 s3, s23, s3
	s_add_i32 s2, s11, 0xeb10
	s_lshl_b32 s23, s2, 1
	s_lshl_b32 s2, s2, 5
	s_and_b32 s2, s2, 0x3e0
	s_and_b32 s31, s23, 0x7fc0
	s_lshl_b32 s23, s2, 2
	v_add_u32_e32 v48, s31, v1
	s_add_u32 s22, s22, s23
	s_addc_u32 s23, s3, 0
	v_ashrrev_i32_e32 v49, 31, v48
	v_lshl_add_u64 v[50:51], s[22:23], 0, v[160:161]
	v_lshlrev_b64 v[48:49], 12, v[48:49]
	v_lshl_add_u64 v[76:77], v[50:51], 0, v[48:49]
	s_mov_b32 s3, 0x8000
	v_add_co_u32_e32 v52, vcc, s3, v76
	s_mov_b32 s3, 0x10000
	s_nop 0
	v_addc_co_u32_e32 v53, vcc, 0, v77, vcc
	v_add_co_u32_e32 v56, vcc, s3, v76
	s_mov_b32 s3, 0x18000
	s_nop 0
	v_addc_co_u32_e32 v57, vcc, 0, v77, vcc
	v_add_co_u32_e32 v60, vcc, s3, v76
	s_mov_b32 s3, 0x20000
	s_nop 0
	v_addc_co_u32_e32 v61, vcc, 0, v77, vcc
	v_add_co_u32_e32 v64, vcc, s3, v76
	s_mov_b32 s3, 0x28000
	s_nop 0
	v_addc_co_u32_e32 v65, vcc, 0, v77, vcc
	v_add_co_u32_e32 v68, vcc, s3, v76
	global_load_dwordx4 v[48:51], v[76:77], off nt
	s_nop 0
	global_load_dwordx4 v[52:55], v[52:53], off nt
	v_addc_co_u32_e32 v69, vcc, 0, v77, vcc
	global_load_dwordx4 v[56:59], v[56:57], off nt
	s_nop 0
	global_load_dwordx4 v[60:63], v[60:61], off nt
	s_nop 0
	global_load_dwordx4 v[64:67], v[64:65], off nt
	s_nop 0
	global_load_dwordx4 v[68:71], v[68:69], off nt
	s_mov_b32 s3, 0x30000
	v_add_co_u32_e32 v72, vcc, s3, v76
	s_mov_b32 s3, 0x38000
	s_nop 0
	v_addc_co_u32_e32 v73, vcc, 0, v77, vcc
	global_load_dwordx4 v[72:75], v[72:73], off nt
	v_add_co_u32_e32 v76, vcc, s3, v76
	v_add_u32_e32 v89, 0x1ce8, v37
	s_nop 0
	v_addc_co_u32_e32 v77, vcc, 0, v77, vcc
	global_load_dwordx4 v[76:79], v[76:77], off nt
	v_add_u32_e32 v80, s2, v1
	v_ashrrev_i32_e32 v81, 31, v80
	s_lshl_b32 s96, s31, 1
	v_lshlrev_b64 v[80:81], 11, v[80:81]
	v_lshl_add_u64 v[84:85], v[2:3], 0, s[96:97]
	v_add_u32_e32 v82, s2, v32
	v_ashrrev_i32_e32 v83, 31, v82
	s_waitcnt vmcnt(7)
	ds_write2_b32 v37, v48, v49 offset1:1
	ds_write2_b32 v37, v50, v51 offset0:2 offset1:3
	s_waitcnt vmcnt(6)
	ds_write2_b32 v38, v52, v53 offset1:1
	ds_write2_b32 v39, v54, v55 offset1:1
	s_waitcnt vmcnt(5)
	ds_write2_b32 v40, v56, v57 offset1:1
	ds_write2_b32 v41, v58, v59 offset1:1
	s_waitcnt vmcnt(4)
	ds_write2_b32 v42, v60, v61 offset1:1
	ds_write2_b32 v43, v62, v63 offset1:1
	s_waitcnt vmcnt(3)
	ds_write2_b32 v44, v64, v65 offset1:1
	ds_write2_b32 v45, v66, v67 offset1:1
	s_waitcnt vmcnt(2)
	ds_write2_b32 v46, v68, v69 offset1:1
	ds_write2_b32 v47, v70, v71 offset1:1
	s_waitcnt vmcnt(1)
	ds_write2_b32 v86, v72, v73 offset1:1
	ds_write2_b32 v87, v74, v75 offset1:1
	s_waitcnt vmcnt(0)
	ds_write2_b32 v88, v76, v77 offset1:1
	ds_write2_b32 v89, v78, v79 offset1:1
	s_waitcnt lgkmcnt(0)
	ds_read2_b32 v[52:53], v36 offset0:33 offset1:41
	ds_read2_b32 v[54:55], v36 offset1:8
	ds_read2_b32 v[56:57], v36 offset0:66 offset1:74
	ds_read2_b32 v[58:59], v36 offset0:99 offset1:107
	ds_read2_b32 v[60:61], v36 offset0:132 offset1:140
	ds_read2_b32 v[62:63], v36 offset0:165 offset1:173
	ds_read2_b32 v[64:65], v36 offset0:198 offset1:206
	ds_read2_b32 v[66:67], v36 offset0:231 offset1:239
	v_lshl_add_u64 v[68:69], v[84:85], 0, v[80:81]
	s_waitcnt lgkmcnt(6)
	v_cvt_pk_bf16_f32 v48, v54, v52
	s_waitcnt lgkmcnt(4)
	v_cvt_pk_bf16_f32 v49, v56, v58
	s_waitcnt lgkmcnt(2)
	v_cvt_pk_bf16_f32 v50, v60, v62
	s_waitcnt lgkmcnt(0)
	v_cvt_pk_bf16_f32 v51, v64, v66
	global_store_dwordx4 v[68:69], v[48:51], off nt
	v_cvt_pk_bf16_f32 v52, v55, v53
	v_cvt_pk_bf16_f32 v53, v57, v59
	v_cvt_pk_bf16_f32 v54, v61, v63
	v_cvt_pk_bf16_f32 v55, v65, v67
	v_lshlrev_b64 v[48:49], 11, v[82:83]
	ds_read2_b32 v[56:57], v36 offset0:49 offset1:57
	ds_read2_b32 v[58:59], v36 offset0:16 offset1:24
	ds_read2_b32 v[60:61], v36 offset0:82 offset1:90
	ds_read2_b32 v[62:63], v36 offset0:115 offset1:123
	ds_read2_b32 v[64:65], v36 offset0:148 offset1:156
	ds_read2_b32 v[66:67], v36 offset0:181 offset1:189
	ds_read2_b32 v[68:69], v36 offset0:214 offset1:222
	ds_read2_b32 v[70:71], v36 offset0:247 offset1:255
	v_lshl_add_u64 v[48:49], v[84:85], 0, v[48:49]
	global_store_dwordx4 v[48:49], v[52:55], off nt
	s_waitcnt lgkmcnt(6)
	v_cvt_pk_bf16_f32 v48, v58, v56
	s_waitcnt lgkmcnt(4)
	v_cvt_pk_bf16_f32 v49, v60, v62
	v_add_u32_e32 v52, s2, v33
	v_ashrrev_i32_e32 v53, 31, v52
	v_lshlrev_b64 v[52:53], 11, v[52:53]
	s_waitcnt lgkmcnt(2)
	v_cvt_pk_bf16_f32 v50, v64, v66
	s_waitcnt lgkmcnt(0)
	v_cvt_pk_bf16_f32 v51, v68, v70
	v_lshl_add_u64 v[52:53], v[84:85], 0, v[52:53]
	global_store_dwordx4 v[52:53], v[48:51], off nt
	v_add_u32_e32 v52, s2, v35
	v_ashrrev_i32_e32 v53, 31, v52
	v_lshlrev_b64 v[52:53], 11, v[52:53]
	v_cvt_pk_bf16_f32 v48, v59, v57
	v_cvt_pk_bf16_f32 v49, v61, v63
	v_cvt_pk_bf16_f32 v50, v65, v67
	v_cvt_pk_bf16_f32 v51, v69, v71
	v_lshl_add_u64 v[52:53], v[84:85], 0, v[52:53]
	global_store_dwordx4 v[52:53], v[48:51], off nt
	s_waitcnt lgkmcnt(0)
	s_mov_b64 s[2:3], 0
.LBB0_27:
	s_andn2_b64 vcc, exec, s[2:3]
	s_cbranch_vccnz .LBB0_29
	v_readlane_b32 s2, v254, 17
	v_lshlrev_b32_e32 v160, 2, v0
	v_add_u32_e32 v86, 0x18c0, v37
	v_mov_b32_e32 v47, s2
	v_readlane_b32 s2, v254, 18
	ds_read_b32 v47, v47
	v_add_u32_e32 v87, 0x18c8, v37
	v_mov_b32_e32 v48, s2
	ds_read_b32 v48, v48
	v_add_u32_e32 v88, 0x1ce0, v37
	s_waitcnt lgkmcnt(1)
	v_readfirstlane_b32 s2, v47
	v_add_u32_e32 v47, 0x14a8, v37
	v_add_u32_e32 v89, 0x1ce8, v37
	s_waitcnt lgkmcnt(0)
	v_readfirstlane_b32 s3, v48
	s_add_u32 s22, s2, s34
	s_addc_u32 s3, s3, s35
	s_add_i32 s2, s11, 0xeb50
	s_and_b32 s23, s2, 0xffff
	s_add_i32 s31, s11, 0xeb30
	s_cmp_lt_u32 s23, 32
	s_cselect_b32 s2, s2, s31
	s_cmp_gt_u32 s23, 31
	s_cselect_b32 s31, 64, 0
	s_lshl_b32 s2, s2, 5
	s_and_b32 s2, s2, 0xffe0
	s_lshl_b32 s23, s2, 2
	v_add_u32_e32 v48, s31, v1
	s_add_u32 s22, s22, s23
	s_addc_u32 s23, s3, 0
	v_ashrrev_i32_e32 v49, 31, v48
	v_lshl_add_u64 v[50:51], s[22:23], 0, v[160:161]
	v_lshlrev_b64 v[48:49], 12, v[48:49]
	v_lshl_add_u64 v[76:77], v[50:51], 0, v[48:49]
	s_mov_b32 s3, 0x8000
	v_add_co_u32_e32 v52, vcc, s3, v76
	s_mov_b32 s3, 0x10000
	s_nop 0
	v_addc_co_u32_e32 v53, vcc, 0, v77, vcc
	v_add_co_u32_e32 v56, vcc, s3, v76
	s_mov_b32 s3, 0x18000
	s_nop 0
	v_addc_co_u32_e32 v57, vcc, 0, v77, vcc
	v_add_co_u32_e32 v60, vcc, s3, v76
	s_mov_b32 s3, 0x20000
	s_nop 0
	v_addc_co_u32_e32 v61, vcc, 0, v77, vcc
	v_add_co_u32_e32 v64, vcc, s3, v76
	s_mov_b32 s3, 0x28000
	s_nop 0
	v_addc_co_u32_e32 v65, vcc, 0, v77, vcc
	v_add_co_u32_e32 v68, vcc, s3, v76
	global_load_dwordx4 v[48:51], v[76:77], off nt
	s_nop 0
	global_load_dwordx4 v[52:55], v[52:53], off nt
	v_addc_co_u32_e32 v69, vcc, 0, v77, vcc
	global_load_dwordx4 v[56:59], v[56:57], off nt
	s_nop 0
	global_load_dwordx4 v[60:63], v[60:61], off nt
	s_nop 0
	global_load_dwordx4 v[64:67], v[64:65], off nt
	s_nop 0
	global_load_dwordx4 v[68:71], v[68:69], off nt
	s_mov_b32 s3, 0x30000
	v_add_co_u32_e32 v72, vcc, s3, v76
	s_mov_b32 s3, 0x38000
	s_nop 0
	v_addc_co_u32_e32 v73, vcc, 0, v77, vcc
	global_load_dwordx4 v[72:75], v[72:73], off nt
	v_add_co_u32_e32 v76, vcc, s3, v76
	v_add_u32_e32 v80, s2, v1
	s_nop 0
	v_addc_co_u32_e32 v77, vcc, 0, v77, vcc
	global_load_dwordx4 v[76:79], v[76:77], off nt
	v_ashrrev_i32_e32 v81, 31, v80
	s_lshl_b32 s96, s31, 1
	v_lshlrev_b64 v[80:81], 9, v[80:81]
	v_lshl_add_u64 v[84:85], v[4:5], 0, s[96:97]
	v_add_u32_e32 v82, s2, v32
	v_ashrrev_i32_e32 v83, 31, v82
	s_waitcnt vmcnt(7)
	ds_write2_b32 v37, v48, v49 offset1:1
	ds_write2_b32 v37, v50, v51 offset0:2 offset1:3
	s_waitcnt vmcnt(6)
	ds_write2_b32 v38, v52, v53 offset1:1
	ds_write2_b32 v39, v54, v55 offset1:1
	s_waitcnt vmcnt(5)
	ds_write2_b32 v40, v56, v57 offset1:1
	ds_write2_b32 v41, v58, v59 offset1:1
	s_waitcnt vmcnt(4)
	ds_write2_b32 v42, v60, v61 offset1:1
	ds_write2_b32 v43, v62, v63 offset1:1
	s_waitcnt vmcnt(3)
	ds_write2_b32 v44, v64, v65 offset1:1
	ds_write2_b32 v45, v66, v67 offset1:1
	s_waitcnt vmcnt(2)
	ds_write2_b32 v46, v68, v69 offset1:1
	ds_write2_b32 v47, v70, v71 offset1:1
	s_waitcnt vmcnt(1)
	ds_write2_b32 v86, v72, v73 offset1:1
	ds_write2_b32 v87, v74, v75 offset1:1
	s_waitcnt vmcnt(0)
	ds_write2_b32 v88, v76, v77 offset1:1
	ds_write2_b32 v89, v78, v79 offset1:1
	s_waitcnt lgkmcnt(0)
	ds_read2_b32 v[52:53], v36 offset0:33 offset1:41
	ds_read2_b32 v[54:55], v36 offset1:8
	ds_read2_b32 v[56:57], v36 offset0:66 offset1:74
	ds_read2_b32 v[58:59], v36 offset0:99 offset1:107
	ds_read2_b32 v[60:61], v36 offset0:132 offset1:140
	ds_read2_b32 v[62:63], v36 offset0:165 offset1:173
	ds_read2_b32 v[64:65], v36 offset0:198 offset1:206
	ds_read2_b32 v[66:67], v36 offset0:231 offset1:239
	v_lshl_add_u64 v[68:69], v[84:85], 0, v[80:81]
	s_waitcnt lgkmcnt(6)
	v_cvt_pk_bf16_f32 v48, v54, v52
	s_waitcnt lgkmcnt(4)
	v_cvt_pk_bf16_f32 v49, v56, v58
	s_waitcnt lgkmcnt(2)
	v_cvt_pk_bf16_f32 v50, v60, v62
	s_waitcnt lgkmcnt(0)
	v_cvt_pk_bf16_f32 v51, v64, v66
	global_store_dwordx4 v[68:69], v[48:51], off nt
	v_cvt_pk_bf16_f32 v52, v55, v53
	v_cvt_pk_bf16_f32 v53, v57, v59
	v_cvt_pk_bf16_f32 v54, v61, v63
	v_cvt_pk_bf16_f32 v55, v65, v67
	v_lshlrev_b64 v[48:49], 9, v[82:83]
	ds_read2_b32 v[56:57], v36 offset0:49 offset1:57
	ds_read2_b32 v[58:59], v36 offset0:16 offset1:24
	ds_read2_b32 v[60:61], v36 offset0:82 offset1:90
	ds_read2_b32 v[62:63], v36 offset0:115 offset1:123
	ds_read2_b32 v[64:65], v36 offset0:148 offset1:156
	ds_read2_b32 v[66:67], v36 offset0:181 offset1:189
	ds_read2_b32 v[68:69], v36 offset0:214 offset1:222
	ds_read2_b32 v[70:71], v36 offset0:247 offset1:255
	v_lshl_add_u64 v[48:49], v[84:85], 0, v[48:49]
	global_store_dwordx4 v[48:49], v[52:55], off nt
	s_waitcnt lgkmcnt(6)
	v_cvt_pk_bf16_f32 v48, v58, v56
	s_waitcnt lgkmcnt(4)
	v_cvt_pk_bf16_f32 v49, v60, v62
	v_add_u32_e32 v52, s2, v33
	v_ashrrev_i32_e32 v53, 31, v52
	v_lshlrev_b64 v[52:53], 9, v[52:53]
	s_waitcnt lgkmcnt(2)
	v_cvt_pk_bf16_f32 v50, v64, v66
	s_waitcnt lgkmcnt(0)
	v_cvt_pk_bf16_f32 v51, v68, v70
	v_lshl_add_u64 v[52:53], v[84:85], 0, v[52:53]
	global_store_dwordx4 v[52:53], v[48:51], off nt
	v_add_u32_e32 v52, s2, v35
	v_ashrrev_i32_e32 v53, 31, v52
	v_lshlrev_b64 v[52:53], 9, v[52:53]
	v_cvt_pk_bf16_f32 v48, v59, v57
	v_cvt_pk_bf16_f32 v49, v61, v63
	v_cvt_pk_bf16_f32 v50, v65, v67
	v_cvt_pk_bf16_f32 v51, v69, v71
	v_lshl_add_u64 v[52:53], v[84:85], 0, v[52:53]
	global_store_dwordx4 v[52:53], v[48:51], off nt
	s_waitcnt lgkmcnt(0)

.LBB0_30:
	s_andn2_b64 vcc, exec, s[2:3]
	s_cbranch_vccnz .LBB0_32
	v_readlane_b32 s2, v254, 19
	v_lshlrev_b32_e32 v160, 2, v0
	v_add_u32_e32 v86, 0x18c0, v37
	v_mov_b32_e32 v47, s2
	v_readlane_b32 s2, v254, 20
	ds_read_b32 v47, v47
	v_add_u32_e32 v87, 0x18c8, v37
	v_mov_b32_e32 v48, s2
	ds_read_b32 v48, v48
	v_add_u32_e32 v88, 0x1ce0, v37
	s_waitcnt lgkmcnt(1)
	v_readfirstlane_b32 s2, v47
	v_add_u32_e32 v89, 0x1ce8, v37
	s_waitcnt lgkmcnt(0)
	v_readfirstlane_b32 s3, v48
	s_add_u32 s2, s2, s40
	s_addc_u32 s3, s3, s41
	s_add_i32 s22, s11, 0xffb0
	s_and_b32 s23, s22, 0xff
	s_mulk_i32 s23, 0xab
	s_bfe_u32 s23, s23, 0x4000c
	s_mul_i32 s31, s23, 24
	s_sub_i32 s22, s22, s31
	s_lshl_b32 s22, s22, 5
	s_lshl_b32 s23, s23, 6
	s_and_b32 s22, s22, 0x1fe0
	s_and_b32 s23, s23, 0x3c0
	s_lshl_b32 s31, s22, 2
	s_add_u32 s2, s2, s31
	v_add_u32_e32 v47, s23, v1
	s_addc_u32 s3, s3, 0
	v_lshl_add_u64 v[76:77], s[2:3], 0, v[160:161]
	s_movk_i32 s31, 0xc00
	v_add_u32_e32 v50, 8, v47
	v_add_u32_e32 v56, 16, v47
	v_add_u32_e32 v58, 24, v47
	v_add_u32_e32 v64, 32, v47
	v_add_u32_e32 v66, 40, v47
	v_mad_i64_i32 v[48:49], s[2:3], v47, s31, v[76:77]
	v_mad_i64_i32 v[52:53], s[2:3], v50, s31, v[76:77]
	v_mad_i64_i32 v[56:57], s[2:3], v56, s31, v[76:77]
	v_mad_i64_i32 v[60:61], s[2:3], v58, s31, v[76:77]
	v_mad_i64_i32 v[64:65], s[2:3], v64, s31, v[76:77]
	v_mad_i64_i32 v[68:69], s[2:3], v66, s31, v[76:77]
	global_load_dwordx4 v[48:51], v[48:49], off nt
	s_nop 0
	global_load_dwordx4 v[52:55], v[52:53], off nt
	s_nop 0
	global_load_dwordx4 v[56:59], v[56:57], off nt
	s_nop 0
	global_load_dwordx4 v[60:63], v[60:61], off nt
	s_nop 0
	global_load_dwordx4 v[64:67], v[64:65], off nt
	s_nop 0
	global_load_dwordx4 v[68:71], v[68:69], off nt
	v_add_u32_e32 v72, 48, v47
	v_mad_i64_i32 v[72:73], s[2:3], v72, s31, v[76:77]
	global_load_dwordx4 v[72:75], v[72:73], off nt
	v_add_u32_e32 v47, 56, v47
	v_mad_i64_i32 v[76:77], s[2:3], v47, s31, v[76:77]
	global_load_dwordx4 v[76:79], v[76:77], off nt
	v_add_u32_e32 v47, 0x14a8, v37
	v_add_u32_e32 v80, s22, v1
	v_ashrrev_i32_e32 v81, 31, v80
	s_lshl_b32 s96, s23, 1
	v_lshlrev_b64 v[80:81], 9, v[80:81]
	v_lshl_add_u64 v[84:85], v[6:7], 0, s[96:97]
	v_add_u32_e32 v82, s22, v32
	v_lshl_add_u64 v[80:81], v[84:85], 0, v[80:81]
	v_ashrrev_i32_e32 v83, 31, v82
	v_lshlrev_b64 v[82:83], 9, v[82:83]
	v_lshl_add_u64 v[82:83], v[84:85], 0, v[82:83]
	s_waitcnt vmcnt(7)
	ds_write2_b32 v37, v48, v49 offset1:1
	ds_write2_b32 v37, v50, v51 offset0:2 offset1:3
	s_waitcnt vmcnt(6)
	ds_write2_b32 v38, v52, v53 offset1:1
	ds_write2_b32 v39, v54, v55 offset1:1
	s_waitcnt vmcnt(5)
	ds_write2_b32 v40, v56, v57 offset1:1
	ds_write2_b32 v41, v58, v59 offset1:1
	s_waitcnt vmcnt(4)
	ds_write2_b32 v42, v60, v61 offset1:1
	ds_write2_b32 v43, v62, v63 offset1:1
	s_waitcnt vmcnt(3)
	ds_write2_b32 v44, v64, v65 offset1:1
	ds_write2_b32 v45, v66, v67 offset1:1
	s_waitcnt vmcnt(2)
	ds_write2_b32 v46, v68, v69 offset1:1
	ds_write2_b32 v47, v70, v71 offset1:1
	s_waitcnt vmcnt(1)
	ds_write2_b32 v86, v72, v73 offset1:1
	ds_write2_b32 v87, v74, v75 offset1:1
	s_waitcnt vmcnt(0)
	ds_write2_b32 v88, v76, v77 offset1:1
	ds_write2_b32 v89, v78, v79 offset1:1
	s_waitcnt lgkmcnt(0)
	ds_read2_b32 v[52:53], v36 offset0:33 offset1:41
	ds_read2_b32 v[54:55], v36 offset1:8
	ds_read2_b32 v[56:57], v36 offset0:66 offset1:74
	ds_read2_b32 v[58:59], v36 offset0:99 offset1:107
	ds_read2_b32 v[60:61], v36 offset0:132 offset1:140
	ds_read2_b32 v[62:63], v36 offset0:165 offset1:173
	ds_read2_b32 v[64:65], v36 offset0:198 offset1:206
	ds_read2_b32 v[66:67], v36 offset0:231 offset1:239
	ds_read2_b32 v[68:69], v36 offset0:49 offset1:57
	ds_read2_b32 v[70:71], v36 offset0:16 offset1:24
	ds_read2_b32 v[72:73], v36 offset0:82 offset1:90
	ds_read2_b32 v[74:75], v36 offset0:115 offset1:123
	ds_read2_b32 v[76:77], v36 offset0:148 offset1:156
	ds_read2_b32 v[78:79], v36 offset0:181 offset1:189
	s_waitcnt lgkmcnt(12)
	v_cvt_pk_bf16_f32 v48, v54, v52
	s_waitcnt lgkmcnt(10)
	v_cvt_pk_bf16_f32 v49, v56, v58
	s_waitcnt lgkmcnt(8)
	v_cvt_pk_bf16_f32 v50, v60, v62
	s_waitcnt lgkmcnt(6)
	v_cvt_pk_bf16_f32 v51, v64, v66
	global_store_dwordx4 v[80:81], v[48:51], off nt
	v_cvt_pk_bf16_f32 v52, v55, v53
	v_cvt_pk_bf16_f32 v53, v57, v59
	ds_read2_b32 v[56:57], v36 offset0:214 offset1:222
	ds_read2_b32 v[58:59], v36 offset0:247 offset1:255
	v_cvt_pk_bf16_f32 v54, v61, v63
	v_cvt_pk_bf16_f32 v55, v65, v67
	global_store_dwordx4 v[82:83], v[52:55], off nt
	s_waitcnt lgkmcnt(6)
	v_cvt_pk_bf16_f32 v48, v70, v68
	s_waitcnt lgkmcnt(4)
	v_cvt_pk_bf16_f32 v49, v72, v74
	v_add_u32_e32 v52, s22, v33
	v_ashrrev_i32_e32 v53, 31, v52
	v_lshlrev_b64 v[52:53], 9, v[52:53]
	s_waitcnt lgkmcnt(2)
	v_cvt_pk_bf16_f32 v50, v76, v78
	s_waitcnt lgkmcnt(0)
	v_cvt_pk_bf16_f32 v51, v56, v58
	v_lshl_add_u64 v[52:53], v[84:85], 0, v[52:53]
	global_store_dwordx4 v[52:53], v[48:51], off nt
	v_add_u32_e32 v52, s22, v35
	v_ashrrev_i32_e32 v53, 31, v52
	v_lshlrev_b64 v[52:53], 9, v[52:53]
	v_cvt_pk_bf16_f32 v48, v71, v69
	v_cvt_pk_bf16_f32 v49, v73, v75
	v_cvt_pk_bf16_f32 v50, v77, v79
	v_cvt_pk_bf16_f32 v51, v57, v59
	v_lshl_add_u64 v[52:53], v[84:85], 0, v[52:53]
	global_store_dwordx4 v[52:53], v[48:51], off nt
	s_waitcnt lgkmcnt(0)

.LBB0_33:
	s_andn2_b64 vcc, exec, s[2:3]
	s_cbranch_vccnz .LBB0_35
	v_readlane_b32 s2, v254, 21
	v_lshlrev_b32_e32 v160, 2, v0
	v_add_u32_e32 v86, 0x18c0, v37
	v_mov_b32_e32 v47, s2
	v_readlane_b32 s2, v254, 22
	ds_read_b32 v47, v47
	v_add_u32_e32 v87, 0x18c8, v37
	v_mov_b32_e32 v48, s2
	ds_read_b32 v48, v48
	s_lshl_b64 s[2:3], s[18:19], 2
	s_waitcnt lgkmcnt(1)
	v_readfirstlane_b32 s22, v47
	v_add_u32_e32 v47, 0x14a8, v37
	v_add_u32_e32 v88, 0x1ce0, v37
	s_waitcnt lgkmcnt(0)
	v_readfirstlane_b32 s23, v48
	s_add_u32 s22, s22, s2
	s_addc_u32 s3, s23, s3
	s_add_i32 s2, s11, 0xedb0
	s_lshl_b32 s23, s2, 1
	s_lshl_b32 s2, s2, 5
	s_and_b32 s2, s2, 0x3e0
	s_and_b32 s31, s23, 0x7fc0
	s_lshl_b32 s23, s2, 2
	v_add_u32_e32 v48, s31, v1
	s_add_u32 s22, s22, s23
	s_addc_u32 s23, s3, 0
	v_ashrrev_i32_e32 v49, 31, v48
	v_lshl_add_u64 v[50:51], s[22:23], 0, v[160:161]
	v_lshlrev_b64 v[48:49], 12, v[48:49]
	v_lshl_add_u64 v[76:77], v[50:51], 0, v[48:49]
	s_mov_b32 s3, 0x8000
	v_add_co_u32_e32 v52, vcc, s3, v76
	s_mov_b32 s3, 0x10000
	s_nop 0
	v_addc_co_u32_e32 v53, vcc, 0, v77, vcc
	v_add_co_u32_e32 v56, vcc, s3, v76
	s_mov_b32 s3, 0x18000
	s_nop 0
	v_addc_co_u32_e32 v57, vcc, 0, v77, vcc
	v_add_co_u32_e32 v60, vcc, s3, v76
	s_mov_b32 s3, 0x20000
	s_nop 0
	v_addc_co_u32_e32 v61, vcc, 0, v77, vcc
	v_add_co_u32_e32 v64, vcc, s3, v76
	s_mov_b32 s3, 0x28000
	s_nop 0
	v_addc_co_u32_e32 v65, vcc, 0, v77, vcc
	v_add_co_u32_e32 v68, vcc, s3, v76
	global_load_dwordx4 v[48:51], v[76:77], off nt
	s_nop 0
	global_load_dwordx4 v[52:55], v[52:53], off nt
	v_addc_co_u32_e32 v69, vcc, 0, v77, vcc
	global_load_dwordx4 v[56:59], v[56:57], off nt
	s_nop 0
	global_load_dwordx4 v[60:63], v[60:61], off nt
	s_nop 0
	global_load_dwordx4 v[64:67], v[64:65], off nt
	s_nop 0
	global_load_dwordx4 v[68:71], v[68:69], off nt
	s_mov_b32 s3, 0x30000
	v_add_co_u32_e32 v72, vcc, s3, v76
	s_mov_b32 s3, 0x38000
	s_nop 0
	v_addc_co_u32_e32 v73, vcc, 0, v77, vcc
	global_load_dwordx4 v[72:75], v[72:73], off nt
	v_add_co_u32_e32 v76, vcc, s3, v76
	v_add_u32_e32 v89, 0x1ce8, v37
	s_nop 0
	v_addc_co_u32_e32 v77, vcc, 0, v77, vcc
	global_load_dwordx4 v[76:79], v[76:77], off nt
	v_add_u32_e32 v80, s2, v1
	v_ashrrev_i32_e32 v81, 31, v80
	s_lshl_b32 s96, s31, 1
	v_lshlrev_b64 v[80:81], 11, v[80:81]
	v_lshl_add_u64 v[84:85], v[8:9], 0, s[96:97]
	v_add_u32_e32 v82, s2, v32
	v_ashrrev_i32_e32 v83, 31, v82
	s_waitcnt vmcnt(7)
	ds_write2_b32 v37, v48, v49 offset1:1
	ds_write2_b32 v37, v50, v51 offset0:2 offset1:3
	s_waitcnt vmcnt(6)
	ds_write2_b32 v38, v52, v53 offset1:1
	ds_write2_b32 v39, v54, v55 offset1:1
	s_waitcnt vmcnt(5)
	ds_write2_b32 v40, v56, v57 offset1:1
	ds_write2_b32 v41, v58, v59 offset1:1
	s_waitcnt vmcnt(4)
	ds_write2_b32 v42, v60, v61 offset1:1
	ds_write2_b32 v43, v62, v63 offset1:1
	s_waitcnt vmcnt(3)
	ds_write2_b32 v44, v64, v65 offset1:1
	ds_write2_b32 v45, v66, v67 offset1:1
	s_waitcnt vmcnt(2)
	ds_write2_b32 v46, v68, v69 offset1:1
	ds_write2_b32 v47, v70, v71 offset1:1
	s_waitcnt vmcnt(1)
	ds_write2_b32 v86, v72, v73 offset1:1
	ds_write2_b32 v87, v74, v75 offset1:1
	s_waitcnt vmcnt(0)
	ds_write2_b32 v88, v76, v77 offset1:1
	ds_write2_b32 v89, v78, v79 offset1:1
	s_waitcnt lgkmcnt(0)
	ds_read2_b32 v[52:53], v36 offset0:33 offset1:41
	ds_read2_b32 v[54:55], v36 offset1:8
	ds_read2_b32 v[56:57], v36 offset0:66 offset1:74
	ds_read2_b32 v[58:59], v36 offset0:99 offset1:107
	ds_read2_b32 v[60:61], v36 offset0:132 offset1:140
	ds_read2_b32 v[62:63], v36 offset0:165 offset1:173
	ds_read2_b32 v[64:65], v36 offset0:198 offset1:206
	ds_read2_b32 v[66:67], v36 offset0:231 offset1:239
	v_lshl_add_u64 v[68:69], v[84:85], 0, v[80:81]
	s_waitcnt lgkmcnt(6)
	v_cvt_pk_bf16_f32 v48, v54, v52
	s_waitcnt lgkmcnt(4)
	v_cvt_pk_bf16_f32 v49, v56, v58
	s_waitcnt lgkmcnt(2)
	v_cvt_pk_bf16_f32 v50, v60, v62
	s_waitcnt lgkmcnt(0)
	v_cvt_pk_bf16_f32 v51, v64, v66
	global_store_dwordx4 v[68:69], v[48:51], off nt
	v_cvt_pk_bf16_f32 v52, v55, v53
	v_cvt_pk_bf16_f32 v53, v57, v59
	v_cvt_pk_bf16_f32 v54, v61, v63
	v_cvt_pk_bf16_f32 v55, v65, v67
	v_lshlrev_b64 v[48:49], 11, v[82:83]
	ds_read2_b32 v[56:57], v36 offset0:49 offset1:57
	ds_read2_b32 v[58:59], v36 offset0:16 offset1:24
	ds_read2_b32 v[60:61], v36 offset0:82 offset1:90
	ds_read2_b32 v[62:63], v36 offset0:115 offset1:123
	ds_read2_b32 v[64:65], v36 offset0:148 offset1:156
	ds_read2_b32 v[66:67], v36 offset0:181 offset1:189
	ds_read2_b32 v[68:69], v36 offset0:214 offset1:222
	ds_read2_b32 v[70:71], v36 offset0:247 offset1:255
	v_lshl_add_u64 v[48:49], v[84:85], 0, v[48:49]
	global_store_dwordx4 v[48:49], v[52:55], off nt
	s_waitcnt lgkmcnt(6)
	v_cvt_pk_bf16_f32 v48, v58, v56
	s_waitcnt lgkmcnt(4)
	v_cvt_pk_bf16_f32 v49, v60, v62
	v_add_u32_e32 v52, s2, v33
	v_ashrrev_i32_e32 v53, 31, v52
	v_lshlrev_b64 v[52:53], 11, v[52:53]
	s_waitcnt lgkmcnt(2)
	v_cvt_pk_bf16_f32 v50, v64, v66
	s_waitcnt lgkmcnt(0)
	v_cvt_pk_bf16_f32 v51, v68, v70
	v_lshl_add_u64 v[52:53], v[84:85], 0, v[52:53]
	global_store_dwordx4 v[52:53], v[48:51], off nt
	v_add_u32_e32 v52, s2, v35
	v_ashrrev_i32_e32 v53, 31, v52
	v_lshlrev_b64 v[52:53], 11, v[52:53]
	v_cvt_pk_bf16_f32 v48, v59, v57
	v_cvt_pk_bf16_f32 v49, v61, v63
	v_cvt_pk_bf16_f32 v50, v65, v67
	v_cvt_pk_bf16_f32 v51, v69, v71
	v_lshl_add_u64 v[52:53], v[84:85], 0, v[52:53]
	global_store_dwordx4 v[52:53], v[48:51], off nt
	s_waitcnt lgkmcnt(0)

.LBB0_36:
	s_andn2_b64 vcc, exec, s[2:3]
	s_cbranch_vccnz .LBB0_38
	v_readlane_b32 s2, v254, 23
	s_add_i32 s31, s11, 0xfffff1b0
	s_lshr_b32 s33, s31, 8
	v_mov_b32_e32 v47, s2
	v_readlane_b32 s2, v254, 24
	ds_read_b32 v47, v47
	s_add_i32 s96, s33, s6
	v_mov_b32_e32 v48, s2
	ds_read_b32 v48, v48
	s_lshl_b64 s[22:23], s[96:97], 21
	s_waitcnt lgkmcnt(1)
	v_readfirstlane_b32 s2, v47
	v_lshlrev_b32_e32 v160, 2, v0
	v_add_u32_e32 v47, 0x14a8, v37
	s_waitcnt lgkmcnt(0)
	v_readfirstlane_b32 s3, v48
	s_add_u32 s2, s2, s22
	s_addc_u32 s3, s3, s23
	s_and_b32 s23, s31, 31
	s_lshl_b32 s22, s33, 10
	s_lshl_b32 s31, s23, 5
	s_or_b32 s22, s22, s31
	s_lshl_b32 s23, s23, 7
	s_add_u32 s2, s2, s23
	s_addc_u32 s3, s3, 0
	v_lshl_add_u64 v[76:77], s[2:3], 0, v[160:161]
	v_lshl_add_u64 v[48:49], v[76:77], 0, v[14:15]
	global_load_dwordx4 v[48:51], v[48:49], off nt
	v_lshl_add_u64 v[52:53], v[76:77], 0, v[16:17]
	global_load_dwordx4 v[52:55], v[52:53], off nt
	v_lshl_add_u64 v[56:57], v[76:77], 0, v[18:19]
	global_load_dwordx4 v[56:59], v[56:57], off nt
	v_lshl_add_u64 v[60:61], v[76:77], 0, v[20:21]
	global_load_dwordx4 v[60:63], v[60:61], off nt
	v_lshl_add_u64 v[64:65], v[76:77], 0, v[22:23]
	global_load_dwordx4 v[64:67], v[64:65], off nt
	v_lshl_add_u64 v[68:69], v[76:77], 0, v[24:25]
	global_load_dwordx4 v[68:71], v[68:69], off nt
	v_lshl_add_u64 v[72:73], v[76:77], 0, v[26:27]
	global_load_dwordx4 v[72:75], v[72:73], off nt
	v_lshl_add_u64 v[76:77], v[76:77], 0, v[28:29]
	global_load_dwordx4 v[76:79], v[76:77], off nt
	v_add_u32_e32 v86, 0x18c0, v37
	v_add_u32_e32 v87, 0x18c8, v37
	v_add_u32_e32 v88, 0x1ce0, v37
	v_add_u32_e32 v89, 0x1ce8, v37
	v_add_u32_e32 v80, s22, v1
	v_add_u32_e32 v82, s22, v32
	v_add_u32_e32 v84, s22, v33
	v_ashrrev_i32_e32 v81, 31, v80
	v_ashrrev_i32_e32 v83, 31, v82
	v_ashrrev_i32_e32 v85, 31, v84
	v_lshlrev_b64 v[80:81], 10, v[80:81]
	v_lshlrev_b64 v[82:83], 10, v[82:83]
	v_lshlrev_b64 v[84:85], 10, v[84:85]
	v_lshl_add_u64 v[80:81], v[30:31], 0, v[80:81]
	v_lshl_add_u64 v[82:83], v[30:31], 0, v[82:83]
	v_lshl_add_u64 v[84:85], v[30:31], 0, v[84:85]
	s_waitcnt vmcnt(7)
	ds_write2_b32 v37, v48, v49 offset1:1
	ds_write2_b32 v37, v50, v51 offset0:2 offset1:3
	s_waitcnt vmcnt(6)
	ds_write2_b32 v38, v52, v53 offset1:1
	ds_write2_b32 v39, v54, v55 offset1:1
	s_waitcnt vmcnt(5)
	ds_write2_b32 v40, v56, v57 offset1:1
	ds_write2_b32 v41, v58, v59 offset1:1
	s_waitcnt vmcnt(4)
	ds_write2_b32 v42, v60, v61 offset1:1
	ds_write2_b32 v43, v62, v63 offset1:1
	s_waitcnt vmcnt(3)
	ds_write2_b32 v44, v64, v65 offset1:1
	ds_write2_b32 v45, v66, v67 offset1:1
	s_waitcnt vmcnt(2)
	ds_write2_b32 v46, v68, v69 offset1:1
	ds_write2_b32 v47, v70, v71 offset1:1
	s_waitcnt vmcnt(1)
	ds_write2_b32 v86, v72, v73 offset1:1
	ds_write2_b32 v87, v74, v75 offset1:1
	s_waitcnt vmcnt(0)
	ds_write2_b32 v88, v76, v77 offset1:1
	ds_write2_b32 v89, v78, v79 offset1:1
	s_waitcnt lgkmcnt(0)
	ds_read2_b32 v[52:53], v36 offset0:33 offset1:41
	ds_read2_b32 v[54:55], v36 offset1:8
	ds_read2_b32 v[56:57], v36 offset0:66 offset1:74
	ds_read2_b32 v[58:59], v36 offset0:99 offset1:107
	ds_read2_b32 v[60:61], v36 offset0:132 offset1:140
	ds_read2_b32 v[62:63], v36 offset0:165 offset1:173
	ds_read2_b32 v[64:65], v36 offset0:198 offset1:206
	ds_read2_b32 v[66:67], v36 offset0:231 offset1:239
	ds_read2_b32 v[68:69], v36 offset0:49 offset1:57
	ds_read2_b32 v[70:71], v36 offset0:16 offset1:24
	ds_read2_b32 v[72:73], v36 offset0:82 offset1:90
	ds_read2_b32 v[74:75], v36 offset0:115 offset1:123
	ds_read2_b32 v[76:77], v36 offset0:148 offset1:156
	ds_read2_b32 v[78:79], v36 offset0:181 offset1:189
	ds_read2_b32 v[86:87], v36 offset0:214 offset1:222
	ds_read2_b32 v[88:89], v36 offset0:247 offset1:255
	s_waitcnt lgkmcnt(14)
	v_cvt_pk_bf16_f32 v48, v54, v52
	s_waitcnt lgkmcnt(12)
	v_cvt_pk_bf16_f32 v49, v56, v58
	s_waitcnt lgkmcnt(10)
	v_cvt_pk_bf16_f32 v50, v60, v62
	s_waitcnt lgkmcnt(8)
	v_cvt_pk_bf16_f32 v51, v64, v66
	v_cvt_pk_bf16_f32 v52, v55, v53
	v_cvt_pk_bf16_f32 v53, v57, v59
	v_cvt_pk_bf16_f32 v54, v61, v63
	v_cvt_pk_bf16_f32 v55, v65, v67
	s_waitcnt lgkmcnt(6)
	v_cvt_pk_bf16_f32 v56, v70, v68
	s_waitcnt lgkmcnt(4)
	v_cvt_pk_bf16_f32 v57, v72, v74
	s_waitcnt lgkmcnt(2)
	v_cvt_pk_bf16_f32 v58, v76, v78
	s_waitcnt lgkmcnt(0)
	v_cvt_pk_bf16_f32 v59, v86, v88
	global_store_dwordx4 v[80:81], v[48:51], off nt
	global_store_dwordx4 v[82:83], v[52:55], off nt
	global_store_dwordx4 v[84:85], v[56:59], off nt
	v_add_u32_e32 v48, s22, v35
	v_ashrrev_i32_e32 v49, 31, v48
	v_lshlrev_b64 v[48:49], 10, v[48:49]
	v_cvt_pk_bf16_f32 v60, v71, v69
	v_cvt_pk_bf16_f32 v61, v73, v75
	v_cvt_pk_bf16_f32 v62, v77, v79
	v_cvt_pk_bf16_f32 v63, v87, v89
	v_lshl_add_u64 v[48:49], v[30:31], 0, v[48:49]
	global_store_dwordx4 v[48:49], v[60:63], off nt
	s_waitcnt lgkmcnt(0)

.LBB0_39:
	s_andn2_b64 vcc, exec, s[2:3]
	s_cbranch_vccnz .LBB0_41
	v_readlane_b32 s2, v254, 25
	v_lshlrev_b32_e32 v160, 2, v0
	s_mov_b32 s4, 0x42000000
	v_mov_b32_e32 v47, s2
	v_readlane_b32 s2, v254, 26
	ds_read_b32 v47, v47
	v_add_u32_e32 v80, 0x18c0, v37
	v_mov_b32_e32 v48, s2
	ds_read_b32 v48, v48
	s_add_i32 s2, s11, 0xfffff9b0
	s_lshr_b32 s31, s2, 9
	s_add_i32 s96, s31, s6
	s_waitcnt lgkmcnt(1)
	v_readfirstlane_b32 s2, v47
	s_waitcnt lgkmcnt(0)
	v_readfirstlane_b32 s3, v48
	s_lshl_b64 s[22:23], s[96:97], 22
	s_add_u32 s22, s2, s22
	s_addc_u32 s3, s3, s23
	s_add_i32 s2, s7, 0xffff3600
	s_and_b32 s23, s2, 0x3e0
	s_lshl_b32 s2, s31, 10
	s_and_b32 s96, s10, 0x3c0
	s_or_b32 s2, s23, s2
	s_lshl_b32 s23, s23, 2
	v_add_u32_e32 v48, s96, v1
	s_add_u32 s22, s22, s23
	s_addc_u32 s23, s3, 0
	v_ashrrev_i32_e32 v49, 31, v48
	v_lshl_add_u64 v[50:51], s[22:23], 0, v[160:161]
	v_lshlrev_b64 v[48:49], 12, v[48:49]
	v_lshl_add_u64 v[76:77], v[50:51], 0, v[48:49]
	s_mov_b32 s3, 0x8000
	v_add_co_u32_e32 v52, vcc, s3, v76
	s_mov_b32 s3, 0x10000
	s_nop 0
	v_addc_co_u32_e32 v53, vcc, 0, v77, vcc
	v_add_co_u32_e32 v56, vcc, s3, v76
	s_mov_b32 s3, 0x18000
	s_nop 0
	v_addc_co_u32_e32 v57, vcc, 0, v77, vcc
	v_add_co_u32_e32 v60, vcc, s3, v76
	s_mov_b32 s3, 0x20000
	s_nop 0
	v_addc_co_u32_e32 v61, vcc, 0, v77, vcc
	v_add_co_u32_e32 v64, vcc, s3, v76
	s_mov_b32 s3, 0x28000
	s_nop 0
	v_addc_co_u32_e32 v65, vcc, 0, v77, vcc
	v_add_co_u32_e32 v68, vcc, s3, v76
	s_mov_b32 s3, 0x30000
	s_nop 0
	v_addc_co_u32_e32 v69, vcc, 0, v77, vcc
	v_add_co_u32_e32 v72, vcc, s3, v76
	s_mov_b32 s3, 0x38000
	s_nop 0
	v_addc_co_u32_e32 v73, vcc, 0, v77, vcc
	global_load_dwordx4 v[48:51], v[76:77], off nt
	s_nop 0
	global_load_dwordx4 v[52:55], v[52:53], off nt
	v_add_co_u32_e32 v76, vcc, s3, v76
	global_load_dwordx4 v[56:59], v[56:57], off nt
	s_nop 0
	global_load_dwordx4 v[60:63], v[60:61], off nt
	v_addc_co_u32_e32 v77, vcc, 0, v77, vcc
	global_load_dwordx4 v[64:67], v[64:65], off nt
	s_nop 0
	global_load_dwordx4 v[68:71], v[68:69], off nt
	v_add_u32_e32 v47, 0x14a8, v37
	global_load_dwordx4 v[72:75], v[72:73], off nt
	v_add_u32_e32 v81, 0x18c8, v37
	global_load_dwordx4 v[76:79], v[76:77], off nt
	v_add_u32_e32 v82, 0x1ce0, v37
	v_add_u32_e32 v83, 0x1ce8, v37
	s_waitcnt vmcnt(7)
	v_pk_mul_f32 v[48:49], v[48:49], s[4:5] op_sel_hi:[1,0]
	v_pk_mul_f32 v[50:51], v[50:51], s[4:5] op_sel_hi:[1,0]
	ds_write2_b32 v37, v48, v49 offset1:1
	ds_write2_b32 v37, v50, v51 offset0:2 offset1:3
	s_waitcnt vmcnt(6)
	v_pk_mul_f32 v[48:49], v[52:53], s[4:5] op_sel_hi:[1,0]
	v_pk_mul_f32 v[50:51], v[54:55], s[4:5] op_sel_hi:[1,0]
	s_waitcnt vmcnt(5)
	v_pk_mul_f32 v[52:53], v[56:57], s[4:5] op_sel_hi:[1,0]
	v_pk_mul_f32 v[54:55], v[58:59], s[4:5] op_sel_hi:[1,0]
	s_waitcnt vmcnt(4)
	v_pk_mul_f32 v[56:57], v[60:61], s[4:5] op_sel_hi:[1,0]
	v_pk_mul_f32 v[58:59], v[62:63], s[4:5] op_sel_hi:[1,0]
	s_waitcnt vmcnt(3)
	v_pk_mul_f32 v[60:61], v[64:65], s[4:5] op_sel_hi:[1,0]
	v_pk_mul_f32 v[62:63], v[66:67], s[4:5] op_sel_hi:[1,0]
	s_waitcnt vmcnt(2)
	v_pk_mul_f32 v[64:65], v[68:69], s[4:5] op_sel_hi:[1,0]
	v_pk_mul_f32 v[66:67], v[70:71], s[4:5] op_sel_hi:[1,0]
	s_waitcnt vmcnt(1)
	v_pk_mul_f32 v[68:69], v[72:73], s[4:5] op_sel_hi:[1,0]
	v_pk_mul_f32 v[70:71], v[74:75], s[4:5] op_sel_hi:[1,0]
	s_waitcnt vmcnt(0)
	v_pk_mul_f32 v[72:73], v[76:77], s[4:5] op_sel_hi:[1,0]
	v_pk_mul_f32 v[74:75], v[78:79], s[4:5] op_sel_hi:[1,0]
	ds_write2_b32 v38, v48, v49 offset1:1
	ds_write2_b32 v39, v50, v51 offset1:1
	ds_write2_b32 v40, v52, v53 offset1:1
	ds_write2_b32 v41, v54, v55 offset1:1
	ds_write2_b32 v42, v56, v57 offset1:1
	ds_write2_b32 v43, v58, v59 offset1:1
	ds_write2_b32 v44, v60, v61 offset1:1
	ds_write2_b32 v45, v62, v63 offset1:1
	ds_write2_b32 v46, v64, v65 offset1:1
	ds_write2_b32 v47, v66, v67 offset1:1
	ds_write2_b32 v80, v68, v69 offset1:1
	ds_write2_b32 v81, v70, v71 offset1:1
	ds_write2_b32 v82, v72, v73 offset1:1
	ds_write2_b32 v83, v74, v75 offset1:1
	s_waitcnt lgkmcnt(0)
	ds_read2_b32 v[48:49], v36 offset0:33 offset1:41
	ds_read2_b32 v[50:51], v36 offset0:66 offset1:74
	ds_read2_b32 v[52:53], v36 offset1:8
	ds_read2_b32 v[54:55], v36 offset0:99 offset1:107
	ds_read2_b32 v[58:59], v36 offset0:132 offset1:140
	ds_read2_b32 v[60:61], v36 offset0:165 offset1:173
	v_mov_b32_e32 v56, v161
	ds_read2_b32 v[62:63], v36 offset0:198 offset1:206
	ds_read2_b32 v[64:65], v36 offset0:231 offset1:239
	v_mov_b32_e32 v57, v161
	s_waitcnt lgkmcnt(5)
	v_cvt_pk_fp8_f32 v56, v52, v48
	s_waitcnt lgkmcnt(2)
	v_cvt_pk_fp8_f32 v57, v58, v60
	v_mov_b32_e32 v48, v161
	v_add_u32_e32 v68, s2, v1
	v_cvt_pk_fp8_f32 v56, v50, v54 op_sel:[0,0,1]
	s_waitcnt lgkmcnt(0)
	v_cvt_pk_fp8_f32 v57, v62, v64 op_sel:[0,0,1]
	v_cvt_pk_fp8_f32 v48, v53, v49
	v_mov_b32_e32 v49, v161
	v_ashrrev_i32_e32 v69, 31, v68
	v_cvt_pk_fp8_f32 v49, v59, v61
	v_lshl_add_u64 v[66:67], v[10:11], 0, s[96:97]
	v_lshlrev_b64 v[68:69], 10, v[68:69]
	v_lshl_add_u64 v[52:53], v[66:67], 0, v[68:69]
	global_store_dwordx2 v[52:53], v[56:57], off nt
	v_cvt_pk_fp8_f32 v48, v51, v55 op_sel:[0,0,1]
	v_cvt_pk_fp8_f32 v49, v63, v65 op_sel:[0,0,1]
	ds_read2_b32 v[52:53], v36 offset0:49 offset1:57
	ds_read2_b32 v[54:55], v36 offset0:82 offset1:90
	ds_read2_b32 v[56:57], v36 offset0:16 offset1:24
	ds_read2_b32 v[58:59], v36 offset0:115 offset1:123
	ds_read2_b32 v[62:63], v36 offset0:148 offset1:156
	ds_read2_b32 v[64:65], v36 offset0:181 offset1:189
	v_add_u32_e32 v50, s2, v32
	v_mov_b32_e32 v60, v161
	ds_read2_b32 v[68:69], v36 offset0:214 offset1:222
	ds_read2_b32 v[70:71], v36 offset0:247 offset1:255
	v_mov_b32_e32 v61, v161
	v_ashrrev_i32_e32 v51, 31, v50
	s_waitcnt lgkmcnt(5)
	v_cvt_pk_fp8_f32 v60, v56, v52
	s_waitcnt lgkmcnt(2)
	v_cvt_pk_fp8_f32 v61, v62, v64
	v_lshlrev_b64 v[50:51], 10, v[50:51]
	v_lshl_add_u64 v[50:51], v[66:67], 0, v[50:51]
	global_store_dwordx2 v[50:51], v[48:49], off nt
	v_mov_b32_e32 v50, v161
	v_mov_b32_e32 v51, v161
	v_cvt_pk_fp8_f32 v60, v54, v58 op_sel:[0,0,1]
	s_waitcnt lgkmcnt(0)
	v_cvt_pk_fp8_f32 v61, v68, v70 op_sel:[0,0,1]
	v_add_u32_e32 v48, s2, v33
	v_cvt_pk_fp8_f32 v50, v57, v53
	v_cvt_pk_fp8_f32 v51, v63, v65
	v_ashrrev_i32_e32 v49, 31, v48
	v_lshlrev_b64 v[48:49], 10, v[48:49]
	v_lshl_add_u64 v[48:49], v[66:67], 0, v[48:49]
	global_store_dwordx2 v[48:49], v[60:61], off nt
	v_cvt_pk_fp8_f32 v50, v55, v59 op_sel:[0,0,1]
	v_cvt_pk_fp8_f32 v51, v69, v71 op_sel:[0,0,1]
	v_add_u32_e32 v48, s2, v35
	v_ashrrev_i32_e32 v49, 31, v48
	v_lshlrev_b64 v[48:49], 10, v[48:49]
	v_lshl_add_u64 v[48:49], v[66:67], 0, v[48:49]
	global_store_dwordx2 v[48:49], v[50:51], off nt
	s_waitcnt lgkmcnt(0)

.LBB0_42:
	s_andn2_b64 vcc, exec, s[2:3]
	s_cbranch_vccnz .LBB0_19
	v_readlane_b32 s22, v254, 27
	s_mul_hi_i32 s2, s11, 0x288df0cb
	s_lshr_b32 s3, s2, 31
	v_mov_b32_e32 v47, s22
	v_readlane_b32 s22, v254, 28
	ds_read_b32 v47, v47
	s_ashr_i32 s2, s2, 4
	v_mov_b32_e32 v48, s22
	ds_read_b32 v48, v48
	s_add_i32 s31, s2, s3
	s_mul_i32 s2, s31, 0xffffff9b
	s_add_i32 s23, s11, s2
	s_waitcnt lgkmcnt(1)
	v_readfirstlane_b32 s2, v47
	s_waitcnt lgkmcnt(0)
	v_readfirstlane_b32 s3, v48
	s_add_u32 s33, s2, s42
	s_mul_i32 s22, s31, 0xfffff360
	s_addc_u32 s3, s3, s43
	s_lshl_b32 s2, s31, 6
	s_add_i32 s22, s7, s22
	s_cmp_gt_i32 s23, 60
	s_cselect_b32 s38, 0x60, 0
	s_ashr_i32 s23, s22, 31
	s_lshl_b64 s[22:23], s[22:23], 2
	s_add_u32 s22, s33, s22
	v_add_u32_e32 v47, s2, v1
	s_addc_u32 s23, s3, s23
	v_lshlrev_b32_e32 v160, 2, v0
	v_lshl_add_u64 v[76:77], s[22:23], 0, v[160:161]
	s_movk_i32 s3, 0x3280
	v_add_u32_e32 v50, 8, v47
	v_add_u32_e32 v56, 16, v47
	v_add_u32_e32 v58, 24, v47
	v_add_u32_e32 v64, 32, v47
	v_add_u32_e32 v66, 40, v47
	v_mad_i64_i32 v[48:49], s[22:23], v47, s3, v[76:77]
	v_mad_i64_i32 v[52:53], s[22:23], v50, s3, v[76:77]
	v_mad_i64_i32 v[56:57], s[22:23], v56, s3, v[76:77]
	v_mad_i64_i32 v[60:61], s[22:23], v58, s3, v[76:77]
	v_mad_i64_i32 v[64:65], s[22:23], v64, s3, v[76:77]
	v_mad_i64_i32 v[68:69], s[22:23], v66, s3, v[76:77]
	global_load_dwordx4 v[48:51], v[48:49], off nt
	s_nop 0
	global_load_dwordx4 v[52:55], v[52:53], off nt
	s_nop 0
	global_load_dwordx4 v[56:59], v[56:57], off nt
	s_nop 0
	global_load_dwordx4 v[60:63], v[60:61], off nt
	s_nop 0
	global_load_dwordx4 v[64:67], v[64:65], off nt
	s_nop 0
	global_load_dwordx4 v[68:71], v[68:69], off nt
	v_add_u32_e32 v72, 48, v47
	v_mad_i64_i32 v[72:73], s[22:23], v72, s3, v[76:77]
	global_load_dwordx4 v[72:75], v[72:73], off nt
	v_add_u32_e32 v47, 56, v47
	v_mad_i64_i32 v[76:77], s[22:23], v47, s3, v[76:77]
	global_load_dwordx4 v[76:79], v[76:77], off nt
	v_add_u32_e32 v47, 0x14a8, v37
	v_add_u32_e32 v86, 0x18c0, v37
	v_add_u32_e32 v87, 0x18c8, v37
	v_add_u32_e32 v88, 0x1ce0, v37
	v_add_u32_e32 v89, 0x1ce8, v37
	s_mulk_i32 s31, 0xca0
	s_sub_i32 s22, s38, s31
	s_add_i32 s22, s22, s7
	v_add_u32_e32 v82, s22, v1
	s_ashr_i32 s3, s2, 31
	v_ashrrev_i32_e32 v83, 31, v82
	v_lshl_add_u64 v[80:81], s[2:3], 1, v[12:13]
	v_lshlrev_b64 v[84:85], 11, v[82:83]
	s_mov_b32 s38, 0x6dc9c883
	s_mov_b32 s39, 0x3fc45f30
	s_waitcnt vmcnt(7)
	ds_write2_b32 v37, v48, v49 offset1:1
	ds_write2_b32 v37, v50, v51 offset0:2 offset1:3
	s_waitcnt vmcnt(6)
	ds_write2_b32 v38, v52, v53 offset1:1
	ds_write2_b32 v39, v54, v55 offset1:1
	s_waitcnt vmcnt(5)
	ds_write2_b32 v40, v56, v57 offset1:1
	ds_write2_b32 v41, v58, v59 offset1:1
	s_waitcnt vmcnt(4)
	ds_write2_b32 v42, v60, v61 offset1:1
	ds_write2_b32 v43, v62, v63 offset1:1
	s_waitcnt vmcnt(3)
	ds_write2_b32 v44, v64, v65 offset1:1
	ds_write2_b32 v45, v66, v67 offset1:1
	s_waitcnt vmcnt(2)
	ds_write2_b32 v46, v68, v69 offset1:1
	ds_write2_b32 v47, v70, v71 offset1:1
	s_waitcnt vmcnt(1)
	ds_write2_b32 v86, v72, v73 offset1:1
	ds_write2_b32 v87, v74, v75 offset1:1
	s_waitcnt vmcnt(0)
	ds_write2_b32 v88, v76, v77 offset1:1
	ds_write2_b32 v89, v78, v79 offset1:1
	s_waitcnt lgkmcnt(0)
	ds_read2_b32 v[52:53], v36 offset0:33 offset1:41
	ds_read2_b32 v[54:55], v36 offset1:8
	ds_read2_b32 v[56:57], v36 offset0:66 offset1:74
	ds_read2_b32 v[58:59], v36 offset0:99 offset1:107
	ds_read2_b32 v[60:61], v36 offset0:132 offset1:140
	ds_read2_b32 v[62:63], v36 offset0:165 offset1:173
	ds_read2_b32 v[64:65], v36 offset0:198 offset1:206
	ds_read2_b32 v[66:67], v36 offset0:231 offset1:239
	v_lshl_add_u64 v[68:69], v[80:81], 0, v[84:85]
	s_waitcnt lgkmcnt(6)
	v_cvt_pk_bf16_f32 v48, v54, v52
	s_waitcnt lgkmcnt(4)
	v_cvt_pk_bf16_f32 v49, v56, v58
	s_waitcnt lgkmcnt(2)
	v_cvt_pk_bf16_f32 v50, v60, v62
	s_waitcnt lgkmcnt(0)
	v_cvt_pk_bf16_f32 v51, v64, v66
	global_store_dwordx4 v[68:69], v[48:51], off nt
	v_cvt_pk_bf16_f32 v52, v55, v53
	v_cvt_pk_bf16_f32 v53, v57, v59
	v_add_u32_e32 v48, 8, v82
	v_ashrrev_i32_e32 v49, 31, v48
	v_cvt_pk_bf16_f32 v54, v61, v63
	v_cvt_pk_bf16_f32 v55, v65, v67
	v_lshlrev_b64 v[48:49], 11, v[48:49]
	ds_read2_b32 v[56:57], v36 offset0:49 offset1:57
	ds_read2_b32 v[58:59], v36 offset0:16 offset1:24
	ds_read2_b32 v[60:61], v36 offset0:82 offset1:90
	ds_read2_b32 v[62:63], v36 offset0:115 offset1:123
	ds_read2_b32 v[64:65], v36 offset0:148 offset1:156
	ds_read2_b32 v[66:67], v36 offset0:181 offset1:189
	ds_read2_b32 v[68:69], v36 offset0:214 offset1:222
	ds_read2_b32 v[70:71], v36 offset0:247 offset1:255
	v_lshl_add_u64 v[48:49], v[80:81], 0, v[48:49]
	global_store_dwordx4 v[48:49], v[52:55], off nt
	s_waitcnt lgkmcnt(6)
	v_cvt_pk_bf16_f32 v48, v58, v56
	s_waitcnt lgkmcnt(4)
	v_cvt_pk_bf16_f32 v49, v60, v62
	v_add_u32_e32 v52, 16, v82
	v_ashrrev_i32_e32 v53, 31, v52
	v_lshlrev_b64 v[52:53], 11, v[52:53]
	s_waitcnt lgkmcnt(2)
	v_cvt_pk_bf16_f32 v50, v64, v66
	s_waitcnt lgkmcnt(0)
	v_cvt_pk_bf16_f32 v51, v68, v70
	v_lshl_add_u64 v[52:53], v[80:81], 0, v[52:53]
	global_store_dwordx4 v[52:53], v[48:51], off nt
	v_add_u32_e32 v52, 24, v82
	v_ashrrev_i32_e32 v53, 31, v52
	v_lshlrev_b64 v[52:53], 11, v[52:53]
	v_cvt_pk_bf16_f32 v48, v59, v57
	v_cvt_pk_bf16_f32 v49, v61, v63
	v_cvt_pk_bf16_f32 v50, v65, v67
	v_cvt_pk_bf16_f32 v51, v69, v71
	v_lshl_add_u64 v[52:53], v[80:81], 0, v[52:53]
	global_store_dwordx4 v[52:53], v[48:51], off nt
	s_waitcnt lgkmcnt(0)
	s_branch .LBB0_19

.LBB0_1159:
	v_mov_b32_e32 v6, s38
	v_mov_b32_e32 v7, s39
	ds_read_b32 v6, v6
	ds_read_b32 v7, v7
	v_mov_b32_e32 v13, s42
	v_readlane_b32 s11, v255, 5
	s_mov_b64 s[40:41], -1
	s_waitcnt lgkmcnt(1)
	v_readfirstlane_b32 s2, v6
	s_waitcnt lgkmcnt(0)
	v_readfirstlane_b32 s3, v7
	ds_read_b32 v6, v13
	v_mov_b32_e32 v7, s43
	ds_read_b32 v7, v7
	s_cmpk_gt_i32 s10, 0xdff
	v_lshlrev_b32_e32 v160, 2, v0
	s_waitcnt lgkmcnt(1)
	v_readfirstlane_b32 s22, v6
	v_mov_b32_e32 v6, s11
	v_readlane_b32 s11, v255, 6
	s_waitcnt lgkmcnt(0)
	v_readfirstlane_b32 s23, v7
	ds_read_b32 v6, v6
	v_mov_b32_e32 v7, s11
	ds_read_b32 v7, v7
	v_add_u32_e32 v13, 0x420, v12
	v_add_u32_e32 v14, 0x428, v12
	s_waitcnt lgkmcnt(1)
	v_readfirstlane_b32 s36, v6
	v_add_u32_e32 v15, 0x840, v12
	s_waitcnt lgkmcnt(0)
	v_readfirstlane_b32 s37, v7
	v_add_u32_e32 v17, 0x848, v12
	v_add_u32_e32 v18, 0xc60, v12
	v_add_u32_e32 v19, 0xc68, v12
	v_add_u32_e32 v20, 0x1080, v12
	v_add_u32_e32 v21, 0x1088, v12
	v_add_u32_e32 v22, 0x14a0, v12
	v_add_u32_e32 v23, 0x14a8, v12
	v_add_u32_e32 v24, 0x18c0, v12
	v_add_u32_e32 v25, 0x18c8, v12
	v_add_u32_e32 v26, 0x1ce0, v12
	v_add_u32_e32 v27, 0x1ce8, v12
	s_cbranch_scc0 .LBB0_1161
	s_and_b32 s11, s6, 0x7fffffc0
	s_add_i32 s96, s11, 0xffffe400
	s_and_b32 s11, s7, 0x3e0
	s_lshl_b32 s19, s11, 2
	v_add_u32_e32 v6, s96, v1
	s_add_u32 s36, s36, s19
	s_addc_u32 s37, s37, 0
	v_ashrrev_i32_e32 v7, 31, v6
	v_lshl_add_u64 v[28:29], s[36:37], 0, v[160:161]
	v_lshlrev_b64 v[6:7], 12, v[6:7]
	v_lshl_add_u64 v[6:7], v[28:29], 0, v[6:7]
	s_mov_b32 s19, 0x8000
	global_load_dwordx4 v[28:31], v[6:7], off nt
	v_add_co_u32_e32 v32, vcc, s19, v6
	s_mov_b32 s19, 0x10000
	s_nop 0
	v_addc_co_u32_e32 v33, vcc, 0, v7, vcc
	global_load_dwordx4 v[32:35], v[32:33], off nt
	v_add_co_u32_e32 v36, vcc, s19, v6
	s_mov_b32 s19, 0x18000
	s_nop 0
	v_addc_co_u32_e32 v37, vcc, 0, v7, vcc
	global_load_dwordx4 v[36:39], v[36:37], off nt
	v_add_co_u32_e32 v40, vcc, s19, v6
	s_mov_b32 s19, 0x20000
	s_nop 0
	v_addc_co_u32_e32 v41, vcc, 0, v7, vcc
	global_load_dwordx4 v[40:43], v[40:41], off nt
	v_add_co_u32_e32 v44, vcc, s19, v6
	s_mov_b32 s19, 0x28000
	s_nop 0
	v_addc_co_u32_e32 v45, vcc, 0, v7, vcc
	global_load_dwordx4 v[44:47], v[44:45], off nt
	v_add_co_u32_e32 v48, vcc, s19, v6
	s_mov_b32 s19, 0x30000
	s_nop 0
	v_addc_co_u32_e32 v49, vcc, 0, v7, vcc
	global_load_dwordx4 v[48:51], v[48:49], off nt
	v_add_co_u32_e32 v52, vcc, s19, v6
	s_mov_b32 s19, 0x38000
	s_nop 0
	v_addc_co_u32_e32 v53, vcc, 0, v7, vcc
	global_load_dwordx4 v[52:55], v[52:53], off nt
	v_add_co_u32_e32 v6, vcc, s19, v6
	s_movk_i32 s19, 0x1c00
	s_nop 0
	v_addc_co_u32_e32 v7, vcc, 0, v7, vcc
	global_load_dwordx4 v[56:59], v[6:7], off nt
	v_lshl_add_u64 v[6:7], s[96:97], 1, v[2:3]
	s_mov_b64 s[40:41], 0
	s_waitcnt vmcnt(7)
	ds_write2_b32 v12, v28, v29 offset1:1
	ds_write2_b32 v12, v30, v31 offset0:2 offset1:3
	s_waitcnt vmcnt(6)
	ds_write2_b32 v13, v32, v33 offset1:1
	ds_write2_b32 v14, v34, v35 offset1:1
	s_waitcnt vmcnt(5)
	ds_write2_b32 v15, v36, v37 offset1:1
	ds_write2_b32 v17, v38, v39 offset1:1
	s_waitcnt vmcnt(4)
	ds_write2_b32 v18, v40, v41 offset1:1
	ds_write2_b32 v19, v42, v43 offset1:1
	s_waitcnt vmcnt(3)
	ds_write2_b32 v20, v44, v45 offset1:1
	ds_write2_b32 v21, v46, v47 offset1:1
	s_waitcnt vmcnt(2)
	ds_write2_b32 v22, v48, v49 offset1:1
	ds_write2_b32 v23, v50, v51 offset1:1
	s_waitcnt vmcnt(1)
	ds_write2_b32 v24, v52, v53 offset1:1
	ds_write2_b32 v25, v54, v55 offset1:1
	s_waitcnt vmcnt(0)
	ds_write2_b32 v26, v56, v57 offset1:1
	ds_write2_b32 v27, v58, v59 offset1:1
	s_waitcnt lgkmcnt(0)
	ds_read2_b32 v[32:33], v11 offset0:33 offset1:41
	ds_read2_b32 v[34:35], v11 offset1:8
	ds_read2_b32 v[36:37], v11 offset0:66 offset1:74
	ds_read2_b32 v[38:39], v11 offset0:99 offset1:107
	ds_read2_b32 v[40:41], v11 offset0:132 offset1:140
	ds_read2_b32 v[42:43], v11 offset0:165 offset1:173
	ds_read2_b32 v[44:45], v11 offset0:198 offset1:206
	ds_read2_b32 v[46:47], v11 offset0:231 offset1:239
	s_waitcnt lgkmcnt(6)
	v_cvt_pk_bf16_f32 v28, v34, v32
	v_add_u32_e32 v32, s11, v1
	s_waitcnt lgkmcnt(4)
	v_cvt_pk_bf16_f32 v29, v36, v38
	s_waitcnt lgkmcnt(2)
	v_cvt_pk_bf16_f32 v30, v40, v42
	s_waitcnt lgkmcnt(0)
	v_cvt_pk_bf16_f32 v31, v44, v46
	v_mad_i64_i32 v[48:49], s[36:37], v32, s19, v[6:7]
	v_add_u32_e32 v32, s11, v8
	global_store_dwordx4 v[48:49], v[28:31], off nt
	s_nop 1
	v_cvt_pk_bf16_f32 v28, v35, v33
	v_cvt_pk_bf16_f32 v29, v37, v39
	v_cvt_pk_bf16_f32 v30, v41, v43
	v_cvt_pk_bf16_f32 v31, v45, v47
	v_mad_i64_i32 v[32:33], s[36:37], v32, s19, v[6:7]
	global_store_dwordx4 v[32:33], v[28:31], off nt
	ds_read2_b32 v[32:33], v11 offset0:49 offset1:57
	ds_read2_b32 v[34:35], v11 offset0:16 offset1:24
	ds_read2_b32 v[36:37], v11 offset0:82 offset1:90
	ds_read2_b32 v[38:39], v11 offset0:115 offset1:123
	ds_read2_b32 v[40:41], v11 offset0:148 offset1:156
	ds_read2_b32 v[42:43], v11 offset0:181 offset1:189
	ds_read2_b32 v[44:45], v11 offset0:214 offset1:222
	ds_read2_b32 v[46:47], v11 offset0:247 offset1:255
	s_waitcnt lgkmcnt(6)
	v_cvt_pk_bf16_f32 v28, v34, v32
	v_add_u32_e32 v32, s11, v9
	s_waitcnt lgkmcnt(4)
	v_cvt_pk_bf16_f32 v29, v36, v38
	s_waitcnt lgkmcnt(2)
	v_cvt_pk_bf16_f32 v30, v40, v42
	s_waitcnt lgkmcnt(0)
	v_cvt_pk_bf16_f32 v31, v44, v46
	v_mad_i64_i32 v[48:49], s[36:37], v32, s19, v[6:7]
	v_add_u32_e32 v32, s11, v10
	global_store_dwordx4 v[48:49], v[28:31], off nt
	v_mad_i64_i32 v[6:7], s[36:37], v32, s19, v[6:7]
	s_nop 0
	v_cvt_pk_bf16_f32 v28, v35, v33
	v_cvt_pk_bf16_f32 v29, v37, v39
	v_cvt_pk_bf16_f32 v30, v41, v43
	v_cvt_pk_bf16_f32 v31, v45, v47
	global_store_dwordx4 v[6:7], v[28:31], off nt
	s_waitcnt lgkmcnt(0)
.LBB0_1161:
	s_andn2_b64 vcc, exec, s[40:41]
	s_cbranch_vccnz .LBB0_1158
	s_mul_hi_i32 s11, s10, 0x92492493
	s_add_i32 s11, s11, s10
	s_lshr_b32 s19, s11, 31
	s_ashr_i32 s11, s11, 10
	s_add_i32 s11, s11, s19
	s_mul_i32 s19, s11, 0xfffff900
	s_add_i32 s19, s10, s19
	s_mul_i32 s31, s19, 0x4925
	s_lshr_b32 s33, s31, 31
	s_ashr_i32 s31, s31, 21
	s_add_i32 s31, s31, s33
	s_sext_i32_i16 s33, s31
	s_mulk_i32 s31, 0x70
	s_sub_i32 s19, s19, s31
	s_add_i32 s31, s10, 0x6ff
	s_sext_i32_i16 s19, s19
	s_cmpk_lt_u32 s31, 0xdff
	s_cselect_b32 s3, s3, s23
	s_cselect_b32 s23, s2, s22
	s_lshl_b32 s36, s19, 5
	s_lshl_b32 s2, s19, 6
	s_and_b32 s2, s2, 0xffffff00
	s_and_b32 s19, s36, 0x60
	s_or_b32 s2, s2, s19
	s_lshl_b32 s11, s11, 7
	s_ashr_i32 s37, s36, 31
	s_lshl_b32 s22, s33, 6
	s_add_i32 s2, s2, s11
	s_lshl_b64 s[36:37], s[36:37], 2
	s_add_u32 s36, s23, s36
	s_addc_u32 s37, s3, s37
	v_add_u32_e32 v56, s22, v1
	v_lshl_add_u64 v[6:7], s[36:37], 0, v[160:161]
	s_movk_i32 s3, 0x3800
	v_mad_i64_i32 v[28:29], s[36:37], v56, s3, v[6:7]
	global_load_dwordx4 v[28:31], v[28:29], off nt
	v_add_u32_e32 v32, 8, v56
	v_mad_i64_i32 v[32:33], s[36:37], v32, s3, v[6:7]
	global_load_dwordx4 v[32:35], v[32:33], off nt
	v_add_u32_e32 v36, 16, v56
	v_mad_i64_i32 v[36:37], s[36:37], v36, s3, v[6:7]
	global_load_dwordx4 v[36:39], v[36:37], off nt
	v_add_u32_e32 v40, 24, v56
	v_mad_i64_i32 v[40:41], s[36:37], v40, s3, v[6:7]
	global_load_dwordx4 v[40:43], v[40:41], off nt
	v_add_u32_e32 v44, 32, v56
	v_mad_i64_i32 v[44:45], s[36:37], v44, s3, v[6:7]
	global_load_dwordx4 v[44:47], v[44:45], off nt
	v_add_u32_e32 v48, 40, v56
	v_mad_i64_i32 v[48:49], s[36:37], v48, s3, v[6:7]
	global_load_dwordx4 v[48:51], v[48:49], off nt
	v_add_u32_e32 v52, 48, v56
	v_mad_i64_i32 v[52:53], s[36:37], v52, s3, v[6:7]
	global_load_dwordx4 v[52:55], v[52:53], off nt
	v_add_u32_e32 v56, 56, v56
	v_mad_i64_i32 v[6:7], s[36:37], v56, s3, v[6:7]
	global_load_dwordx4 v[56:59], v[6:7], off nt
	s_ashr_i32 s23, s22, 31
	v_lshl_add_u64 v[6:7], s[22:23], 1, v[4:5]
	s_waitcnt vmcnt(7)
	ds_write2_b32 v12, v28, v29 offset1:1
	ds_write2_b32 v12, v30, v31 offset0:2 offset1:3
	s_waitcnt vmcnt(6)
	ds_write2_b32 v13, v32, v33 offset1:1
	ds_write2_b32 v14, v34, v35 offset1:1
	s_waitcnt vmcnt(5)
	ds_write2_b32 v15, v36, v37 offset1:1
	ds_write2_b32 v17, v38, v39 offset1:1
	s_waitcnt vmcnt(4)
	ds_write2_b32 v18, v40, v41 offset1:1
	ds_write2_b32 v19, v42, v43 offset1:1
	s_waitcnt vmcnt(3)
	ds_write2_b32 v20, v44, v45 offset1:1
	ds_write2_b32 v21, v46, v47 offset1:1
	s_waitcnt vmcnt(2)
	ds_write2_b32 v22, v48, v49 offset1:1
	ds_write2_b32 v23, v50, v51 offset1:1
	s_waitcnt vmcnt(1)
	ds_write2_b32 v24, v52, v53 offset1:1
	ds_write2_b32 v25, v54, v55 offset1:1
	s_waitcnt vmcnt(0)
	ds_write2_b32 v26, v56, v57 offset1:1
	ds_write2_b32 v27, v58, v59 offset1:1
	s_waitcnt lgkmcnt(0)
	ds_read2_b32 v[14:15], v11 offset0:33 offset1:41
	ds_read2_b32 v[22:23], v11 offset1:8
	ds_read2_b32 v[24:25], v11 offset0:66 offset1:74
	ds_read2_b32 v[26:27], v11 offset0:99 offset1:107
	ds_read2_b32 v[28:29], v11 offset0:132 offset1:140
	ds_read2_b32 v[30:31], v11 offset0:165 offset1:173
	ds_read2_b32 v[32:33], v11 offset0:198 offset1:206
	ds_read2_b32 v[34:35], v11 offset0:231 offset1:239
	v_add_u32_e32 v36, s2, v1
	v_ashrrev_i32_e32 v37, 31, v36
	v_lshlrev_b64 v[36:37], 11, v[36:37]
	s_waitcnt lgkmcnt(6)
	v_cvt_pk_bf16_f32 v18, v22, v14
	s_waitcnt lgkmcnt(4)
	v_cvt_pk_bf16_f32 v19, v24, v26
	s_waitcnt lgkmcnt(2)
	v_cvt_pk_bf16_f32 v20, v28, v30
	s_waitcnt lgkmcnt(0)
	v_cvt_pk_bf16_f32 v21, v32, v34
	v_lshl_add_u64 v[36:37], v[6:7], 0, v[36:37]
	v_add_u32_e32 v14, s2, v8
	global_store_dwordx4 v[36:37], v[18:21], off nt
	v_add_u32_e32 v36, s2, v9
	v_ashrrev_i32_e32 v37, 31, v36
	v_cvt_pk_bf16_f32 v18, v23, v15
	v_ashrrev_i32_e32 v15, 31, v14
	v_lshlrev_b64 v[14:15], 11, v[14:15]
	v_cvt_pk_bf16_f32 v19, v25, v27
	v_cvt_pk_bf16_f32 v20, v29, v31
	v_cvt_pk_bf16_f32 v21, v33, v35
	v_lshl_add_u64 v[14:15], v[6:7], 0, v[14:15]
	global_store_dwordx4 v[14:15], v[18:21], off nt
	ds_read2_b32 v[14:15], v11 offset0:49 offset1:57
	ds_read2_b32 v[22:23], v11 offset0:16 offset1:24
	ds_read2_b32 v[24:25], v11 offset0:82 offset1:90
	ds_read2_b32 v[26:27], v11 offset0:115 offset1:123
	ds_read2_b32 v[28:29], v11 offset0:148 offset1:156
	ds_read2_b32 v[30:31], v11 offset0:181 offset1:189
	ds_read2_b32 v[32:33], v11 offset0:214 offset1:222
	ds_read2_b32 v[34:35], v11 offset0:247 offset1:255
	v_lshlrev_b64 v[36:37], 11, v[36:37]
	s_waitcnt lgkmcnt(6)
	v_cvt_pk_bf16_f32 v18, v22, v14
	s_waitcnt lgkmcnt(4)
	v_cvt_pk_bf16_f32 v19, v24, v26
	s_waitcnt lgkmcnt(2)
	v_cvt_pk_bf16_f32 v20, v28, v30
	s_waitcnt lgkmcnt(0)
	v_cvt_pk_bf16_f32 v21, v32, v34
	v_lshl_add_u64 v[36:37], v[6:7], 0, v[36:37]
	v_add_u32_e32 v14, s2, v10
	global_store_dwordx4 v[36:37], v[18:21], off nt
	s_nop 1
	v_cvt_pk_bf16_f32 v18, v23, v15
	v_ashrrev_i32_e32 v15, 31, v14
	v_lshlrev_b64 v[14:15], 11, v[14:15]
	v_cvt_pk_bf16_f32 v19, v25, v27
	v_cvt_pk_bf16_f32 v20, v29, v31
	v_cvt_pk_bf16_f32 v21, v33, v35
	v_lshl_add_u64 v[6:7], v[6:7], 0, v[14:15]
	global_store_dwordx4 v[6:7], v[18:21], off nt
	s_waitcnt lgkmcnt(0)
	s_branch .LBB0_1158

.LBB0_1377:
	v_readlane_b32 s3, v255, 9
	s_mul_hi_i32 s2, s38, 0x30c30c31
	s_ashr_i32 s44, s2, 10
	v_mov_b32_e32 v4, s3
	v_readlane_b32 s3, v255, 10
	ds_read_b32 v4, v4
	s_mov_b64 s[22:23], -1
	v_mov_b32_e32 v5, s3
	ds_read_b32 v5, v5
	s_lshr_b32 s3, s2, 31
	v_readlane_b32 s2, v255, 11
	s_waitcnt lgkmcnt(1)
	v_readfirstlane_b32 s18, v4
	s_add_i32 s44, s44, s3
	s_waitcnt lgkmcnt(0)
	v_readfirstlane_b32 s19, v5
	v_mov_b32_e32 v4, s2
	v_readlane_b32 s2, v255, 12
	ds_read_b32 v4, v4
	s_mul_i32 s3, s44, 0xa80000
	v_mov_b32_e32 v5, s2
	ds_read_b32 v5, v5
	s_add_u32 s39, s10, s3
	v_readlane_b32 s3, v255, 13
	s_waitcnt lgkmcnt(1)
	v_readfirstlane_b32 s36, v4
	s_mul_hi_i32 s2, s44, 0xa80000
	v_mov_b32_e32 v4, s3
	v_readlane_b32 s3, v255, 14
	s_waitcnt lgkmcnt(0)
	v_readfirstlane_b32 s37, v5
	ds_read_b32 v4, v4
	v_mov_b32_e32 v5, s3
	ds_read_b32 v5, v5
	s_addc_u32 s40, s11, s2
	s_mul_i32 s2, s44, 0xffffeb00
	s_add_i32 s41, s38, s2
	s_waitcnt lgkmcnt(1)
	v_readfirstlane_b32 s2, v4
	s_waitcnt lgkmcnt(0)
	v_readfirstlane_b32 s3, v5
	s_cmpk_gt_i32 s41, 0xdff
	s_mul_hi_i32 s42, s44, 0xe00000
	s_mul_i32 s43, s44, 0xe00000
	v_lshlrev_b32_e32 v160, 2, v0
	v_add_u32_e32 v37, 0x420, v23
	v_add_u32_e32 v36, 0x428, v23
	v_add_u32_e32 v35, 0x840, v23
	v_add_u32_e32 v34, 0x848, v23
	v_add_u32_e32 v33, 0xc60, v23
	v_add_u32_e32 v32, 0xc68, v23
	v_add_u32_e32 v31, 0x1080, v23
	v_add_u32_e32 v30, 0x1088, v23
	v_add_u32_e32 v29, 0x14a0, v23
	v_add_u32_e32 v28, 0x14a8, v23
	v_add_u32_e32 v27, 0x18c0, v23
	v_add_u32_e32 v26, 0x18c8, v23
	v_add_u32_e32 v25, 0x1ce0, v23
	v_add_u32_e32 v24, 0x1ce8, v23
	s_cbranch_scc0 .LBB0_1379
	s_add_u32 s22, s2, s43
	s_mulk_i32 s44, 0xd600
	s_addc_u32 s3, s3, s42
	s_add_i32 s2, s33, s44
	s_and_b32 s2, s2, 0x7fffffc0
	s_add_i32 s44, s2, 0xffffe400
	s_and_b32 s2, s31, 0x3e0
	s_lshl_b32 s23, s2, 2
	v_add_u32_e32 v4, s44, v1
	s_add_u32 s22, s22, s23
	s_addc_u32 s23, s3, 0
	v_ashrrev_i32_e32 v5, 31, v4
	v_lshl_add_u64 v[6:7], s[22:23], 0, v[160:161]
	v_lshlrev_b64 v[4:5], 12, v[4:5]
	v_lshl_add_u64 v[18:19], v[6:7], 0, v[4:5]
	s_mov_b32 s3, 0x8000
	global_load_dwordx4 v[4:7], v[18:19], off nt
	v_add_co_u32_e32 v10, vcc, s3, v18
	s_mov_b32 s3, 0x10000
	s_nop 0
	v_addc_co_u32_e32 v11, vcc, 0, v19, vcc
	global_load_dwordx4 v[10:13], v[10:11], off nt
	v_add_co_u32_e32 v14, vcc, s3, v18
	s_mov_b32 s3, 0x18000
	s_nop 0
	v_addc_co_u32_e32 v15, vcc, 0, v19, vcc
	global_load_dwordx4 v[14:17], v[14:15], off nt
	v_add_co_u32_e32 v38, vcc, s3, v18
	s_mov_b32 s3, 0x20000
	s_nop 0
	v_addc_co_u32_e32 v39, vcc, 0, v19, vcc
	global_load_dwordx4 v[38:41], v[38:39], off nt
	v_add_co_u32_e32 v42, vcc, s3, v18
	s_mov_b32 s3, 0x28000
	s_nop 0
	v_addc_co_u32_e32 v43, vcc, 0, v19, vcc
	global_load_dwordx4 v[42:45], v[42:43], off nt
	v_add_co_u32_e32 v46, vcc, s3, v18
	s_mov_b32 s3, 0x30000
	s_nop 0
	v_addc_co_u32_e32 v47, vcc, 0, v19, vcc
	global_load_dwordx4 v[46:49], v[46:47], off nt
	v_add_co_u32_e32 v50, vcc, s3, v18
	s_mov_b32 s3, 0x38000
	s_nop 0
	v_addc_co_u32_e32 v51, vcc, 0, v19, vcc
	global_load_dwordx4 v[50:53], v[50:51], off nt
	v_add_co_u32_e32 v18, vcc, s3, v18
	s_mov_b32 s4, 0x42800000
	s_nop 0
	v_addc_co_u32_e32 v19, vcc, 0, v19, vcc
	global_load_dwordx4 v[54:57], v[18:19], off nt
	s_add_u32 s22, s39, s44
	s_addc_u32 s23, s40, 0
	s_movk_i32 s3, 0xe00
	s_waitcnt vmcnt(7)
	v_pk_mul_f32 v[4:5], v[4:5], s[4:5] op_sel_hi:[1,0]
	ds_write2_b32 v23, v4, v5 offset1:1
	v_pk_mul_f32 v[4:5], v[6:7], s[4:5] op_sel_hi:[1,0]
	ds_write2_b32 v23, v4, v5 offset0:2 offset1:3
	s_waitcnt vmcnt(6)
	v_pk_mul_f32 v[4:5], v[10:11], s[4:5] op_sel_hi:[1,0]
	ds_write2_b32 v37, v4, v5 offset1:1
	v_pk_mul_f32 v[4:5], v[12:13], s[4:5] op_sel_hi:[1,0]
	ds_write2_b32 v36, v4, v5 offset1:1
	s_waitcnt vmcnt(5)
	v_pk_mul_f32 v[4:5], v[14:15], s[4:5] op_sel_hi:[1,0]
	ds_write2_b32 v35, v4, v5 offset1:1
	v_pk_mul_f32 v[4:5], v[16:17], s[4:5] op_sel_hi:[1,0]
	ds_write2_b32 v34, v4, v5 offset1:1
	s_waitcnt vmcnt(4)
	v_pk_mul_f32 v[4:5], v[38:39], s[4:5] op_sel_hi:[1,0]
	ds_write2_b32 v33, v4, v5 offset1:1
	v_pk_mul_f32 v[4:5], v[40:41], s[4:5] op_sel_hi:[1,0]
	ds_write2_b32 v32, v4, v5 offset1:1
	v_mov_b32_e32 v38, v161
	v_mov_b32_e32 v39, v161
	s_waitcnt vmcnt(3)
	v_pk_mul_f32 v[4:5], v[42:43], s[4:5] op_sel_hi:[1,0]
	ds_write2_b32 v31, v4, v5 offset1:1
	v_pk_mul_f32 v[4:5], v[44:45], s[4:5] op_sel_hi:[1,0]
	ds_write2_b32 v30, v4, v5 offset1:1
	s_waitcnt vmcnt(2)
	v_pk_mul_f32 v[4:5], v[46:47], s[4:5] op_sel_hi:[1,0]
	ds_write2_b32 v29, v4, v5 offset1:1
	v_pk_mul_f32 v[4:5], v[48:49], s[4:5] op_sel_hi:[1,0]
	ds_write2_b32 v28, v4, v5 offset1:1
	s_waitcnt vmcnt(1)
	v_pk_mul_f32 v[4:5], v[50:51], s[4:5] op_sel_hi:[1,0]
	ds_write2_b32 v27, v4, v5 offset1:1
	v_pk_mul_f32 v[4:5], v[52:53], s[4:5] op_sel_hi:[1,0]
	ds_write2_b32 v26, v4, v5 offset1:1
	s_waitcnt vmcnt(0)
	v_pk_mul_f32 v[4:5], v[54:55], s[4:5] op_sel_hi:[1,0]
	ds_write2_b32 v25, v4, v5 offset1:1
	v_pk_mul_f32 v[4:5], v[56:57], s[4:5] op_sel_hi:[1,0]
	ds_write2_b32 v24, v4, v5 offset1:1
	s_waitcnt lgkmcnt(0)
	ds_read2_b32 v[6:7], v22 offset0:33 offset1:41
	ds_read2_b32 v[10:11], v22 offset0:66 offset1:74
	ds_read2_b32 v[12:13], v22 offset0:99 offset1:107
	ds_read2_b32 v[14:15], v22 offset1:8
	v_lshl_add_u64 v[4:5], s[22:23], 0, v[2:3]
	s_mov_b64 s[4:5], 0x700000
	v_lshl_add_u64 v[4:5], v[4:5], 0, s[4:5]
	ds_read2_b32 v[40:41], v22 offset0:132 offset1:140
	ds_read2_b32 v[42:43], v22 offset0:165 offset1:173
	ds_read2_b32 v[16:17], v22 offset0:198 offset1:206
	ds_read2_b32 v[18:19], v22 offset0:231 offset1:239
	s_waitcnt lgkmcnt(4)
	v_cvt_pk_fp8_f32 v38, v14, v6
	v_add_u32_e32 v6, s2, v1
	v_mad_i64_i32 v[44:45], s[22:23], v6, s3, v[4:5]
	v_mov_b32_e32 v6, v161
	v_cvt_pk_fp8_f32 v6, v15, v7
	v_mov_b32_e32 v7, v161
	s_waitcnt lgkmcnt(2)
	v_cvt_pk_fp8_f32 v39, v40, v42
	v_cvt_pk_fp8_f32 v7, v41, v43
	v_cvt_pk_fp8_f32 v38, v10, v12 op_sel:[0,0,1]
	v_cvt_pk_fp8_f32 v6, v11, v13 op_sel:[0,0,1]
	s_waitcnt lgkmcnt(0)
	v_cvt_pk_fp8_f32 v39, v16, v18 op_sel:[0,0,1]
	v_cvt_pk_fp8_f32 v7, v17, v19 op_sel:[0,0,1]
	v_add_u32_e32 v10, s2, v9
	v_mad_i64_i32 v[10:11], s[22:23], v10, s3, v[4:5]
	global_store_dwordx2 v[44:45], v[38:39], off nt
	global_store_dwordx2 v[10:11], v[6:7], off nt
	ds_read2_b32 v[6:7], v22 offset0:49 offset1:57
	ds_read2_b32 v[10:11], v22 offset0:82 offset1:90
	ds_read2_b32 v[12:13], v22 offset0:115 offset1:123
	ds_read2_b32 v[14:15], v22 offset0:16 offset1:24
	v_mov_b32_e32 v16, v161
	ds_read2_b32 v[18:19], v22 offset0:148 offset1:156
	ds_read2_b32 v[38:39], v22 offset0:181 offset1:189
	ds_read2_b32 v[40:41], v22 offset0:214 offset1:222
	ds_read2_b32 v[42:43], v22 offset0:247 offset1:255
	v_mov_b32_e32 v17, v161
	s_waitcnt lgkmcnt(4)
	v_cvt_pk_fp8_f32 v16, v14, v6
	v_add_u32_e32 v6, s2, v20
	v_mad_i64_i32 v[44:45], s[22:23], v6, s3, v[4:5]
	v_mov_b32_e32 v6, v161
	v_cvt_pk_fp8_f32 v6, v15, v7
	v_mov_b32_e32 v7, v161
	s_waitcnt lgkmcnt(2)
	v_cvt_pk_fp8_f32 v17, v18, v38
	v_cvt_pk_fp8_f32 v7, v19, v39
	v_cvt_pk_fp8_f32 v16, v10, v12 op_sel:[0,0,1]
	v_cvt_pk_fp8_f32 v6, v11, v13 op_sel:[0,0,1]
	s_waitcnt lgkmcnt(0)
	v_cvt_pk_fp8_f32 v17, v40, v42 op_sel:[0,0,1]
	v_cvt_pk_fp8_f32 v7, v41, v43 op_sel:[0,0,1]
	v_add_u32_e32 v10, s2, v21
	v_mad_i64_i32 v[4:5], s[2:3], v10, s3, v[4:5]
	global_store_dwordx2 v[44:45], v[16:17], off nt
	global_store_dwordx2 v[4:5], v[6:7], off nt
	s_waitcnt lgkmcnt(0)
	s_mov_b64 s[22:23], 0
.LBB0_1379:
	s_andn2_b64 vcc, exec, s[22:23]
	s_cbranch_vccnz .LBB0_1376
	s_mul_i32 s2, s41, 0x4925
	s_lshr_b32 s3, s2, 31
	s_ashr_i32 s2, s2, 25
	s_add_i32 s2, s2, s3
	s_sext_i32_i16 s3, s2
	s_mulk_i32 s2, 0x700
	s_sub_i32 s2, s41, s2
	s_sext_i32_i16 s22, s2
	s_mulk_i32 s22, 0x4925
	s_lshr_b32 s23, s22, 31
	s_ashr_i32 s22, s22, 21
	s_add_i32 s22, s22, s23
	s_sext_i32_i16 s23, s22
	s_mulk_i32 s22, 0x70
	s_sub_i32 s2, s2, s22
	s_addk_i32 s41, 0x6ff
	s_cmpk_lt_u32 s41, 0xdff
	s_cselect_b32 s18, s18, s36
	s_sext_i32_i16 s2, s2
	s_cselect_b32 s19, s19, s37
	s_add_u32 s22, s18, s43
	s_addc_u32 s36, s19, s42
	s_lshl_b32 s18, s2, 5
	s_lshl_b32 s2, s2, 6
	s_and_b32 s2, s2, 0xffffff00
	s_and_b32 s19, s18, 0x60
	s_or_b32 s2, s2, s19
	s_lshl_b32 s3, s3, 7
	s_ashr_i32 s19, s18, 31
	s_lshl_b32 s23, s23, 6
	s_add_i32 s2, s2, s3
	s_lshl_b64 s[18:19], s[18:19], 2
	s_add_u32 s18, s22, s18
	s_addc_u32 s19, s36, s19
	v_add_u32_e32 v54, s23, v1
	v_lshl_add_u64 v[18:19], s[18:19], 0, v[160:161]
	s_movk_i32 s3, 0x3800
	v_mad_i64_i32 v[4:5], s[18:19], v54, s3, v[18:19]
	global_load_dwordx4 v[4:7], v[4:5], off nt
	v_add_u32_e32 v10, 8, v54
	v_mad_i64_i32 v[10:11], s[18:19], v10, s3, v[18:19]
	global_load_dwordx4 v[10:13], v[10:11], off nt
	v_add_u32_e32 v14, 16, v54
	v_mad_i64_i32 v[14:15], s[18:19], v14, s3, v[18:19]
	global_load_dwordx4 v[14:17], v[14:15], off nt
	v_add_u32_e32 v38, 24, v54
	v_mad_i64_i32 v[38:39], s[18:19], v38, s3, v[18:19]
	global_load_dwordx4 v[38:41], v[38:39], off nt
	v_add_u32_e32 v42, 32, v54
	v_mad_i64_i32 v[42:43], s[18:19], v42, s3, v[18:19]
	global_load_dwordx4 v[42:45], v[42:43], off nt
	v_add_u32_e32 v46, 40, v54
	v_mad_i64_i32 v[46:47], s[18:19], v46, s3, v[18:19]
	global_load_dwordx4 v[46:49], v[46:47], off nt
	v_add_u32_e32 v50, 48, v54
	v_mad_i64_i32 v[50:51], s[18:19], v50, s3, v[18:19]
	global_load_dwordx4 v[50:53], v[50:51], off nt
	v_add_u32_e32 v54, 56, v54
	v_mad_i64_i32 v[18:19], s[18:19], v54, s3, v[18:19]
	global_load_dwordx4 v[54:57], v[18:19], off nt
	s_mov_b32 s4, 0x42000000
	s_ashr_i32 s3, s23, 31
	s_add_u32 s18, s39, s23
	s_addc_u32 s19, s40, s3
	s_waitcnt vmcnt(7)
	v_pk_mul_f32 v[4:5], v[4:5], s[4:5] op_sel_hi:[1,0]
	ds_write2_b32 v23, v4, v5 offset1:1
	v_pk_mul_f32 v[4:5], v[6:7], s[4:5] op_sel_hi:[1,0]
	ds_write2_b32 v23, v4, v5 offset0:2 offset1:3
	s_waitcnt vmcnt(6)
	v_pk_mul_f32 v[4:5], v[10:11], s[4:5] op_sel_hi:[1,0]
	ds_write2_b32 v37, v4, v5 offset1:1
	v_pk_mul_f32 v[4:5], v[12:13], s[4:5] op_sel_hi:[1,0]
	ds_write2_b32 v36, v4, v5 offset1:1
	s_waitcnt vmcnt(5)
	v_pk_mul_f32 v[4:5], v[14:15], s[4:5] op_sel_hi:[1,0]
	ds_write2_b32 v35, v4, v5 offset1:1
	v_pk_mul_f32 v[4:5], v[16:17], s[4:5] op_sel_hi:[1,0]
	ds_write2_b32 v34, v4, v5 offset1:1
	s_waitcnt vmcnt(4)
	v_pk_mul_f32 v[4:5], v[38:39], s[4:5] op_sel_hi:[1,0]
	ds_write2_b32 v33, v4, v5 offset1:1
	v_pk_mul_f32 v[4:5], v[40:41], s[4:5] op_sel_hi:[1,0]
	ds_write2_b32 v32, v4, v5 offset1:1
	s_waitcnt vmcnt(3)
	v_pk_mul_f32 v[4:5], v[42:43], s[4:5] op_sel_hi:[1,0]
	ds_write2_b32 v31, v4, v5 offset1:1
	v_pk_mul_f32 v[4:5], v[44:45], s[4:5] op_sel_hi:[1,0]
	ds_write2_b32 v30, v4, v5 offset1:1
	s_waitcnt vmcnt(2)
	v_pk_mul_f32 v[4:5], v[46:47], s[4:5] op_sel_hi:[1,0]
	ds_write2_b32 v29, v4, v5 offset1:1
	v_pk_mul_f32 v[4:5], v[48:49], s[4:5] op_sel_hi:[1,0]
	ds_write2_b32 v28, v4, v5 offset1:1
	s_waitcnt vmcnt(1)
	v_pk_mul_f32 v[4:5], v[50:51], s[4:5] op_sel_hi:[1,0]
	ds_write2_b32 v27, v4, v5 offset1:1
	v_pk_mul_f32 v[4:5], v[52:53], s[4:5] op_sel_hi:[1,0]
	ds_write2_b32 v26, v4, v5 offset1:1
	s_waitcnt vmcnt(0)
	v_pk_mul_f32 v[4:5], v[54:55], s[4:5] op_sel_hi:[1,0]
	ds_write2_b32 v25, v4, v5 offset1:1
	v_pk_mul_f32 v[4:5], v[56:57], s[4:5] op_sel_hi:[1,0]
	ds_write2_b32 v24, v4, v5 offset1:1
	s_waitcnt lgkmcnt(0)
	ds_read2_b32 v[6:7], v22 offset0:33 offset1:41
	ds_read2_b32 v[10:11], v22 offset0:66 offset1:74
	ds_read2_b32 v[12:13], v22 offset0:99 offset1:107
	ds_read2_b32 v[14:15], v22 offset1:8
	v_mov_b32_e32 v16, v161
	ds_read2_b32 v[18:19], v22 offset0:132 offset1:140
	ds_read2_b32 v[24:25], v22 offset0:165 offset1:173
	ds_read2_b32 v[26:27], v22 offset0:198 offset1:206
	ds_read2_b32 v[28:29], v22 offset0:231 offset1:239
	v_mov_b32_e32 v17, v161
	v_add_u32_e32 v30, s2, v1
	s_waitcnt lgkmcnt(4)
	v_cvt_pk_fp8_f32 v16, v14, v6
	v_mov_b32_e32 v6, v161
	v_cvt_pk_fp8_f32 v6, v15, v7
	v_mov_b32_e32 v7, v161
	s_waitcnt lgkmcnt(2)
	v_cvt_pk_fp8_f32 v17, v18, v24
	v_cvt_pk_fp8_f32 v7, v19, v25
	v_cvt_pk_fp8_f32 v16, v10, v12 op_sel:[0,0,1]
	v_cvt_pk_fp8_f32 v6, v11, v13 op_sel:[0,0,1]
	s_waitcnt lgkmcnt(0)
	v_cvt_pk_fp8_f32 v17, v26, v28 op_sel:[0,0,1]
	v_cvt_pk_fp8_f32 v7, v27, v29 op_sel:[0,0,1]
	v_add_u32_e32 v10, s2, v9
	v_ashrrev_i32_e32 v31, 31, v30
	v_ashrrev_i32_e32 v11, 31, v10
	v_lshl_add_u64 v[4:5], s[18:19], 0, v[2:3]
	v_lshlrev_b64 v[30:31], 10, v[30:31]
	v_lshlrev_b64 v[10:11], 10, v[10:11]
	v_lshl_add_u64 v[30:31], v[4:5], 0, v[30:31]
	v_lshl_add_u64 v[10:11], v[4:5], 0, v[10:11]
	global_store_dwordx2 v[30:31], v[16:17], off nt
	global_store_dwordx2 v[10:11], v[6:7], off nt
	ds_read2_b32 v[6:7], v22 offset0:49 offset1:57
	ds_read2_b32 v[10:11], v22 offset0:82 offset1:90
	ds_read2_b32 v[12:13], v22 offset0:115 offset1:123
	ds_read2_b32 v[14:15], v22 offset0:16 offset1:24
	v_mov_b32_e32 v16, v161
	ds_read2_b32 v[18:19], v22 offset0:148 offset1:156
	ds_read2_b32 v[24:25], v22 offset0:181 offset1:189
	ds_read2_b32 v[26:27], v22 offset0:214 offset1:222
	ds_read2_b32 v[28:29], v22 offset0:247 offset1:255
	v_mov_b32_e32 v17, v161
	v_add_u32_e32 v30, s2, v20
	s_waitcnt lgkmcnt(4)
	v_cvt_pk_fp8_f32 v16, v14, v6
	v_mov_b32_e32 v6, v161
	v_cvt_pk_fp8_f32 v6, v15, v7
	v_mov_b32_e32 v7, v161
	s_waitcnt lgkmcnt(2)
	v_cvt_pk_fp8_f32 v17, v18, v24
	v_cvt_pk_fp8_f32 v7, v19, v25
	v_cvt_pk_fp8_f32 v16, v10, v12 op_sel:[0,0,1]
	v_cvt_pk_fp8_f32 v6, v11, v13 op_sel:[0,0,1]
	s_waitcnt lgkmcnt(0)
	v_cvt_pk_fp8_f32 v17, v26, v28 op_sel:[0,0,1]
	v_cvt_pk_fp8_f32 v7, v27, v29 op_sel:[0,0,1]
	v_add_u32_e32 v10, s2, v21
	v_ashrrev_i32_e32 v31, 31, v30
	v_ashrrev_i32_e32 v11, 31, v10
	v_lshlrev_b64 v[30:31], 10, v[30:31]
	v_lshlrev_b64 v[10:11], 10, v[10:11]
	v_lshl_add_u64 v[30:31], v[4:5], 0, v[30:31]
	v_lshl_add_u64 v[4:5], v[4:5], 0, v[10:11]
	global_store_dwordx2 v[30:31], v[16:17], off nt
	global_store_dwordx2 v[4:5], v[6:7], off nt
	s_waitcnt lgkmcnt(0)
	s_branch .LBB0_1376
